# accumulator zeroing in front of GEMM tiles with v_mov_b64 (half the instructions)
# baseline (speedup 1.0000x reference)
.LBB0_257:
	s_lshl_b32 s10, s10, 7
	v_and_b32_e32 v1, 15, v0
	v_and_b32_e32 v2, 48, v0
	v_lshlrev_b32_e32 v0, 2, v0
	s_add_i32 s36, s20, s10
	s_lshl_b32 s27, s31, 7
	v_lshl_or_b32 v1, v1, 6, v2
	v_and_b32_e32 v0, 32, v0
	v_bitop3_b32 v165, v1, s27, v0 bitop3:0xde
	s_add_u32 s27, s76, 0x64c00000
	s_addc_u32 s33, s77, 0
	s_add_u32 s58, s76, 0x9f710000
	s_addc_u32 s59, s77, 0
	s_add_u32 s6, s6, 0x80
	s_waitcnt vmcnt(2)
	s_barrier
	s_addc_u32 s7, s7, 0
	s_mov_b32 m0, s44
	s_nop 4
	global_load_lds_dwordx4 v162, s[6:7]
	s_mov_b32 m0, s45
	s_nop 4
	global_load_lds_dwordx4 v164, s[6:7]
	s_add_u32 s6, s18, 0x80
	s_addc_u32 s7, s19, 0
	s_mov_b32 m0, s46
	s_nop 4
	global_load_lds_dwordx4 v161, s[6:7]
	s_mov_b32 m0, s47
	s_nop 4
	global_load_lds_dwordx4 v163, s[6:7]
	s_add_u32 s6, s21, 0x100080
	s_addc_u32 s7, s60, 0
	s_mov_b32 m0, s48
	s_nop 4
	global_load_lds_dwordx4 v162, s[6:7]
	s_mov_b32 m0, s49
	s_nop 4
	global_load_lds_dwordx4 v164, s[6:7]
	s_waitcnt vmcnt(6)
	s_waitcnt vmcnt(6)
	v_bitop3_b32 v76, v1, s22, v0 bitop3:0xde
	s_mov_b32 s60, 0
	v_add_u32_e32 v166, s91, v76
	s_mov_b32 s64, s11
	s_mov_b32 s62, s20
	s_barrier
	v_mov_b64 v[148:149], 0
	v_mov_b64 v[150:151], 0
	v_mov_b64 v[144:145], 0
	v_mov_b64 v[146:147], 0
	v_mov_b64 v[132:133], 0
	v_mov_b64 v[134:135], 0
	v_mov_b64 v[128:129], 0
	v_mov_b64 v[130:131], 0
	v_mov_b64 v[104:105], 0
	v_mov_b64 v[106:107], 0
	v_mov_b64 v[92:93], 0
	v_mov_b64 v[94:95], 0
	v_mov_b64 v[68:69], 0
	v_mov_b64 v[70:71], 0
	s_waitcnt vmcnt(1)
	v_mov_b64 v[60:61], 0
	s_waitcnt vmcnt(0)
	v_mov_b64 v[62:63], 0
	v_mov_b64 v[156:157], 0
	v_mov_b64 v[158:159], 0
	v_mov_b64 v[152:153], 0
	v_mov_b64 v[154:155], 0
	v_mov_b64 v[140:141], 0
	v_mov_b64 v[142:143], 0
	v_mov_b64 v[136:137], 0
	v_mov_b64 v[138:139], 0
	v_mov_b64 v[124:125], 0
	v_mov_b64 v[126:127], 0
	v_mov_b64 v[112:113], 0
	v_mov_b64 v[114:115], 0
	v_mov_b64 v[80:81], 0
	v_mov_b64 v[82:83], 0
	v_mov_b64 v[72:73], 0
	v_mov_b64 v[74:75], 0
	v_mov_b64 v[52:53], 0
	v_mov_b64 v[54:55], 0
	v_mov_b64 v[48:49], 0
	v_mov_b64 v[50:51], 0
	v_mov_b64 v[36:37], 0
	v_mov_b64 v[38:39], 0
	v_mov_b64 v[32:33], 0
	v_mov_b64 v[34:35], 0
	v_mov_b64 v[20:21], 0
	v_mov_b64 v[22:23], 0
	v_mov_b64 v[16:17], 0
	v_mov_b64 v[18:19], 0
	v_mov_b64 v[4:5], 0
	v_mov_b64 v[6:7], 0
	v_mov_b64 v[0:1], 0
	v_mov_b64 v[2:3], 0
	v_mov_b64 v[64:65], 0
	v_mov_b64 v[66:67], 0
	v_mov_b64 v[56:57], 0
	v_mov_b64 v[58:59], 0
	v_mov_b64 v[44:45], 0
	v_mov_b64 v[46:47], 0
	v_mov_b64 v[40:41], 0
	v_mov_b64 v[42:43], 0
	v_mov_b64 v[28:29], 0
	v_mov_b64 v[30:31], 0
	v_mov_b64 v[24:25], 0
	v_mov_b64 v[26:27], 0
	v_mov_b64 v[12:13], 0
	v_mov_b64 v[14:15], 0
	v_mov_b64 v[8:9], 0
	v_mov_b64 v[10:11], 0
	s_branch .LBB0_260

.LBB0_266:
	s_ashr_i32 s11, s10, 31
	s_lshl_b64 s[10:11], s[10:11], 2
	s_add_u32 s18, s8, s10
	v_mbcnt_lo_u32_b32 v167, -1, 0
	v_mbcnt_hi_u32_b32 v167, -1, v167
	s_addc_u32 s19, s9, s11
	v_lshrrev_b32_e32 v76, 1, v167
	v_and_or_b32 v168, v76, 24, s31
	s_add_u32 s10, s58, s10
	v_lshlrev_b32_e32 v200, 2, v168
	s_addc_u32 s11, s59, s11
	v_lshl_add_u64 v[84:85], s[18:19], 0, v[200:201]
	v_lshl_add_u64 v[96:97], s[10:11], 0, v[200:201]
	global_load_dwordx4 v[76:79], v200, s[18:19] offset:16
	global_load_dwordx4 v[100:103], v200, s[18:19]
	global_load_dwordx4 v[88:91], v200, s[10:11] offset:16
	global_load_dwordx4 v[116:119], v200, s[10:11]
	s_mov_b64 s[10:11], 0x1000
	v_lshl_add_u64 v[86:87], v[84:85], 0, s[10:11]
	v_lshl_add_u64 v[98:99], v[96:97], 0, s[10:11]
	s_movk_i32 s10, 0x1000
	v_add_co_u32_e32 v84, vcc, s10, v84
	v_and_or_b32 v167, v167, 15, s55
	s_nop 0
	v_addc_co_u32_e32 v85, vcc, 0, v85, vcc
	v_add_co_u32_e32 v96, vcc, s10, v96
	global_load_dwordx4 v[108:111], v[84:85], off
	s_nop 0
	global_load_dwordx4 v[84:87], v[86:87], off offset:16
	v_addc_co_u32_e32 v97, vcc, 0, v97, vcc
	global_load_dwordx4 v[120:123], v[96:97], off
	s_nop 0
	global_load_dwordx4 v[96:99], v[98:99], off offset:16
	s_lshl_b64 s[10:11], s[36:37], 1
	s_add_u32 s10, s27, s10
	s_addc_u32 s11, s33, s11
	v_lshl_or_b32 v200, v167, 10, v168
	s_andn2_b64 vcc, exec, s[6:7]
	s_waitcnt vmcnt(5)
	v_fma_f32 v144, v144, v88, v76
	s_waitcnt vmcnt(4)
	v_fma_f32 v148, v148, v116, v100
	v_fma_f32 v132, v132, v116, v100
	v_fma_f32 v104, v104, v116, v100
	v_fma_f32 v68, v68, v116, v100
	v_fma_f32 v128, v128, v88, v76
	v_fma_f32 v92, v92, v88, v76
	v_fma_f32 v60, v60, v88, v76
	v_fma_f32 v52, v52, v116, v100
	v_fma_f32 v36, v36, v116, v100
	v_fma_f32 v20, v20, v116, v100
	v_fma_f32 v4, v4, v116, v100
	v_fma_f32 v48, v48, v88, v76
	v_fma_f32 v32, v32, v88, v76
	v_fma_f32 v16, v16, v88, v76
	s_waitcnt vmcnt(1)
	v_fma_f32 v156, v156, v120, v108
	v_mul_f32_e32 v156, 0xbfb8aa3b, v156
	v_exp_f32_e32 v156, v156
	v_fma_f32 v140, v140, v120, v108
	v_mul_f32_e32 v140, 0xbfb8aa3b, v140
	v_exp_f32_e32 v140, v140
	v_fma_f32 v124, v124, v120, v108
	v_mul_f32_e32 v124, 0xbfb8aa3b, v124
	v_add_f32_e32 v156, 1.0, v156
	v_exp_f32_e32 v124, v124
	v_fma_f32 v80, v80, v120, v108
	v_rcp_f32_e32 v156, v156
	v_mul_f32_e32 v80, 0xbfb8aa3b, v80
	v_add_f32_e32 v140, 1.0, v140
	v_exp_f32_e32 v80, v80
	v_rcp_f32_e32 v140, v140
	v_add_f32_e32 v124, 1.0, v124
	v_mul_f32_e32 v156, v148, v156
	v_fma_f32 v148, v149, v117, v101
	v_fma_f32 v149, v157, v121, v109
	v_rcp_f32_e32 v124, v124
	v_mul_f32_e32 v149, 0xbfb8aa3b, v149
	v_add_f32_e32 v80, 1.0, v80
	v_exp_f32_e32 v149, v149
	v_mul_f32_e32 v140, v132, v140
	v_fma_f32 v132, v133, v117, v101
	v_fma_f32 v133, v141, v121, v109
	v_rcp_f32_e32 v80, v80
	v_mul_f32_e32 v133, 0xbfb8aa3b, v133
	v_exp_f32_e32 v133, v133
	v_mul_f32_e32 v124, v104, v124
	v_fma_f32 v104, v105, v117, v101
	v_fma_f32 v105, v125, v121, v109
	v_mul_f32_e32 v105, 0xbfb8aa3b, v105
	v_add_f32_e32 v149, 1.0, v149
	v_exp_f32_e32 v105, v105
	v_mul_f32_e32 v80, v68, v80
	v_fma_f32 v68, v69, v117, v101
	v_fma_f32 v69, v81, v121, v109
	v_rcp_f32_e32 v149, v149
	v_mul_f32_e32 v69, 0xbfb8aa3b, v69
	v_add_f32_e32 v133, 1.0, v133
	v_exp_f32_e32 v69, v69
	v_rcp_f32_e32 v133, v133
	v_add_f32_e32 v105, 1.0, v105
	v_mul_f32_e32 v157, v148, v149
	v_fma_f32 v149, v158, v122, v110
	v_rcp_f32_e32 v105, v105
	v_mul_f32_e32 v149, 0xbfb8aa3b, v149
	v_add_f32_e32 v69, 1.0, v69
	v_exp_f32_e32 v149, v149
	v_mul_f32_e32 v141, v132, v133
	v_fma_f32 v133, v142, v122, v110
	v_rcp_f32_e32 v69, v69
	v_mul_f32_e32 v133, 0xbfb8aa3b, v133
	v_exp_f32_e32 v133, v133
	v_mul_f32_e32 v125, v104, v105
	v_fma_f32 v105, v126, v122, v110
	v_mul_f32_e32 v105, 0xbfb8aa3b, v105
	v_add_f32_e32 v149, 1.0, v149
	v_exp_f32_e32 v105, v105
	v_mul_f32_e32 v81, v68, v69
	v_fma_f32 v69, v82, v122, v110
	v_rcp_f32_e32 v149, v149
	v_mul_f32_e32 v69, 0xbfb8aa3b, v69
	v_add_f32_e32 v133, 1.0, v133
	v_exp_f32_e32 v69, v69
	v_rcp_f32_e32 v133, v133
	v_fma_f32 v148, v150, v118, v102
	v_add_f32_e32 v105, 1.0, v105
	v_mul_f32_e32 v150, v148, v149
	v_fma_f32 v149, v159, v123, v111
	v_rcp_f32_e32 v105, v105
	v_mul_f32_e32 v149, 0xbfb8aa3b, v149
	v_fma_f32 v132, v134, v118, v102
	v_add_f32_e32 v69, 1.0, v69
	v_exp_f32_e32 v149, v149
	v_mul_f32_e32 v134, v132, v133
	v_fma_f32 v133, v143, v123, v111
	v_rcp_f32_e32 v69, v69
	v_mul_f32_e32 v133, 0xbfb8aa3b, v133
	v_fma_f32 v104, v106, v118, v102
	v_exp_f32_e32 v133, v133
	v_mul_f32_e32 v106, v104, v105
	v_fma_f32 v105, v127, v123, v111
	v_mul_f32_e32 v105, 0xbfb8aa3b, v105
	v_fma_f32 v68, v70, v118, v102
	v_add_f32_e32 v149, 1.0, v149
	v_exp_f32_e32 v105, v105
	v_mul_f32_e32 v70, v68, v69
	v_fma_f32 v69, v83, v123, v111
	v_rcp_f32_e32 v149, v149
	v_mul_f32_e32 v69, 0xbfb8aa3b, v69
	v_add_f32_e32 v133, 1.0, v133
	v_exp_f32_e32 v69, v69
	v_rcp_f32_e32 v133, v133
	v_fma_f32 v148, v151, v119, v103
	v_add_f32_e32 v105, 1.0, v105
	v_mul_f32_e32 v151, v148, v149
	s_waitcnt vmcnt(0)
	v_fma_f32 v148, v152, v96, v84
	v_rcp_f32_e32 v105, v105
	v_mul_f32_e32 v148, 0xbfb8aa3b, v148
	v_fma_f32 v132, v135, v119, v103
	v_add_f32_e32 v69, 1.0, v69
	v_exp_f32_e32 v148, v148
	v_mul_f32_e32 v135, v132, v133
	v_fma_f32 v132, v136, v96, v84
	v_rcp_f32_e32 v69, v69
	v_mul_f32_e32 v132, 0xbfb8aa3b, v132
	v_fma_f32 v104, v107, v119, v103
	v_exp_f32_e32 v132, v132
	v_mul_f32_e32 v107, v104, v105
	v_fma_f32 v104, v112, v96, v84
	v_mul_f32_e32 v104, 0xbfb8aa3b, v104
	v_fma_f32 v68, v71, v119, v103
	v_add_f32_e32 v148, 1.0, v148
	v_exp_f32_e32 v104, v104
	v_mul_f32_e32 v71, v68, v69
	v_fma_f32 v68, v72, v96, v84
	v_rcp_f32_e32 v148, v148
	v_mul_f32_e32 v68, 0xbfb8aa3b, v68
	v_add_f32_e32 v132, 1.0, v132
	v_exp_f32_e32 v68, v68
	v_rcp_f32_e32 v132, v132
	v_add_f32_e32 v104, 1.0, v104
	v_mul_f32_e32 v152, v144, v148
	v_fma_f32 v144, v145, v89, v77
	v_fma_f32 v145, v153, v97, v85
	v_rcp_f32_e32 v104, v104
	v_mul_f32_e32 v145, 0xbfb8aa3b, v145
	v_add_f32_e32 v68, 1.0, v68
	v_exp_f32_e32 v145, v145
	v_mul_f32_e32 v136, v128, v132
	v_fma_f32 v128, v129, v89, v77
	v_fma_f32 v129, v137, v97, v85
	v_rcp_f32_e32 v68, v68
	v_mul_f32_e32 v129, 0xbfb8aa3b, v129
	v_exp_f32_e32 v129, v129
	v_mul_f32_e32 v112, v92, v104
	v_fma_f32 v92, v93, v89, v77
	v_fma_f32 v93, v113, v97, v85
	v_mul_f32_e32 v93, 0xbfb8aa3b, v93
	v_add_f32_e32 v145, 1.0, v145
	v_exp_f32_e32 v93, v93
	v_mul_f32_e32 v72, v60, v68
	v_fma_f32 v60, v61, v89, v77
	v_fma_f32 v61, v73, v97, v85
	v_rcp_f32_e32 v145, v145
	v_mul_f32_e32 v61, 0xbfb8aa3b, v61
	v_add_f32_e32 v129, 1.0, v129
	v_exp_f32_e32 v61, v61
	v_rcp_f32_e32 v129, v129
	v_add_f32_e32 v93, 1.0, v93
	v_mul_f32_e32 v153, v144, v145
	v_fma_f32 v145, v154, v98, v86
	v_rcp_f32_e32 v93, v93
	v_mul_f32_e32 v145, 0xbfb8aa3b, v145
	v_add_f32_e32 v61, 1.0, v61
	v_exp_f32_e32 v145, v145
	v_mul_f32_e32 v137, v128, v129
	v_fma_f32 v129, v138, v98, v86
	v_rcp_f32_e32 v61, v61
	v_mul_f32_e32 v129, 0xbfb8aa3b, v129
	v_exp_f32_e32 v129, v129
	v_mul_f32_e32 v113, v92, v93
	v_fma_f32 v93, v114, v98, v86
	v_mul_f32_e32 v93, 0xbfb8aa3b, v93
	v_add_f32_e32 v145, 1.0, v145
	v_exp_f32_e32 v93, v93
	v_mul_f32_e32 v73, v60, v61
	v_fma_f32 v61, v74, v98, v86
	v_rcp_f32_e32 v145, v145
	v_mul_f32_e32 v61, 0xbfb8aa3b, v61
	v_add_f32_e32 v129, 1.0, v129
	v_exp_f32_e32 v61, v61
	v_rcp_f32_e32 v129, v129
	v_fma_f32 v144, v146, v90, v78
	v_add_f32_e32 v93, 1.0, v93
	v_mul_f32_e32 v154, v144, v145
	v_fma_f32 v145, v155, v99, v87
	v_rcp_f32_e32 v93, v93
	v_mul_f32_e32 v145, 0xbfb8aa3b, v145
	v_fma_f32 v128, v130, v90, v78
	v_add_f32_e32 v61, 1.0, v61
	v_exp_f32_e32 v145, v145
	v_mul_f32_e32 v138, v128, v129
	v_fma_f32 v129, v139, v99, v87
	v_rcp_f32_e32 v61, v61
	v_mul_f32_e32 v129, 0xbfb8aa3b, v129
	v_fma_f32 v92, v94, v90, v78
	v_exp_f32_e32 v129, v129
	v_mul_f32_e32 v114, v92, v93
	v_fma_f32 v93, v115, v99, v87
	v_mul_f32_e32 v93, 0xbfb8aa3b, v93
	v_fma_f32 v60, v62, v90, v78
	v_add_f32_e32 v145, 1.0, v145
	v_exp_f32_e32 v93, v93
	v_mul_f32_e32 v74, v60, v61
	v_fma_f32 v61, v75, v99, v87
	v_rcp_f32_e32 v145, v145
	v_mul_f32_e32 v61, 0xbfb8aa3b, v61
	v_add_f32_e32 v129, 1.0, v129
	v_exp_f32_e32 v61, v61
	v_rcp_f32_e32 v129, v129
	v_fma_f32 v144, v147, v91, v79
	v_add_f32_e32 v93, 1.0, v93
	v_mul_f32_e32 v147, v144, v145
	v_lshl_add_u64 v[148:149], v[200:201], 1, s[10:11]
	v_cvt_pk_bf16_f32 v144, v156, v157
	v_cvt_pk_bf16_f32 v145, v150, v151
	v_rcp_f32_e32 v93, v93
	v_cvt_pk_bf16_f32 v146, v152, v153
	v_cvt_pk_bf16_f32 v147, v154, v147
	global_store_dwordx4 v[148:149], v[144:147], off
	v_fma_f32 v128, v131, v91, v79
	v_add_f32_e32 v61, 1.0, v61
	v_or_b32_e32 v144, 0x4000, v200
	v_mov_b32_e32 v145, v201
	v_mul_f32_e32 v131, v128, v129
	v_lshl_add_u64 v[132:133], v[144:145], 1, s[10:11]
	v_cvt_pk_bf16_f32 v128, v140, v141
	v_cvt_pk_bf16_f32 v129, v134, v135
	v_rcp_f32_e32 v61, v61
	v_cvt_pk_bf16_f32 v130, v136, v137
	v_cvt_pk_bf16_f32 v131, v138, v131
	global_store_dwordx4 v[132:133], v[128:131], off
	v_fma_f32 v92, v95, v91, v79
	v_mul_f32_e32 v95, v92, v93
	v_or_b32_e32 v128, 0x8000, v200
	v_mov_b32_e32 v129, v201
	v_lshl_add_u64 v[104:105], v[128:129], 1, s[10:11]
	v_cvt_pk_bf16_f32 v92, v124, v125
	v_cvt_pk_bf16_f32 v93, v106, v107
	v_cvt_pk_bf16_f32 v94, v112, v113
	v_cvt_pk_bf16_f32 v95, v114, v95
	global_store_dwordx4 v[104:105], v[92:95], off
	v_fma_f32 v60, v63, v91, v79
	v_mul_f32_e32 v63, v60, v61
	v_or_b32_e32 v92, 0xc000, v200
	v_mov_b32_e32 v93, v201
	v_lshl_add_u64 v[68:69], v[92:93], 1, s[10:11]
	v_cvt_pk_bf16_f32 v60, v80, v81
	v_cvt_pk_bf16_f32 v61, v70, v71
	v_cvt_pk_bf16_f32 v62, v72, v73
	v_cvt_pk_bf16_f32 v63, v74, v63
	global_store_dwordx4 v[68:69], v[60:63], off
	v_fma_f32 v44, v44, v120, v108
	v_mul_f32_e32 v44, 0xbfb8aa3b, v44
	v_fma_f32 v62, v64, v120, v108
	v_mul_f32_e32 v62, 0xbfb8aa3b, v62
	v_exp_f32_e32 v62, v62
	v_exp_f32_e32 v44, v44
	v_fma_f32 v28, v28, v120, v108
	v_mul_f32_e32 v28, 0xbfb8aa3b, v28
	v_add_f32_e32 v62, 1.0, v62
	v_exp_f32_e32 v28, v28
	v_fma_f32 v12, v12, v120, v108
	v_rcp_f32_e32 v62, v62
	v_mul_f32_e32 v12, 0xbfb8aa3b, v12
	v_add_f32_e32 v44, 1.0, v44
	v_exp_f32_e32 v12, v12
	v_rcp_f32_e32 v44, v44
	v_add_f32_e32 v28, 1.0, v28
	v_mul_f32_e32 v62, v52, v62
	v_fma_f32 v52, v53, v117, v101
	v_fma_f32 v53, v65, v121, v109
	v_rcp_f32_e32 v28, v28
	v_mul_f32_e32 v53, 0xbfb8aa3b, v53
	v_add_f32_e32 v12, 1.0, v12
	v_exp_f32_e32 v53, v53
	v_mul_f32_e32 v44, v36, v44
	v_fma_f32 v36, v37, v117, v101
	v_fma_f32 v37, v45, v121, v109
	v_rcp_f32_e32 v12, v12
	v_mul_f32_e32 v37, 0xbfb8aa3b, v37
	v_exp_f32_e32 v37, v37
	v_mul_f32_e32 v28, v20, v28
	v_fma_f32 v20, v21, v117, v101
	v_fma_f32 v21, v29, v121, v109
	v_mul_f32_e32 v21, 0xbfb8aa3b, v21
	v_add_f32_e32 v53, 1.0, v53
	v_exp_f32_e32 v21, v21
	v_mul_f32_e32 v12, v4, v12
	v_fma_f32 v4, v5, v117, v101
	v_fma_f32 v5, v13, v121, v109
	v_rcp_f32_e32 v53, v53
	v_mul_f32_e32 v5, 0xbfb8aa3b, v5
	v_add_f32_e32 v37, 1.0, v37
	v_exp_f32_e32 v5, v5
	v_rcp_f32_e32 v37, v37
	v_add_f32_e32 v21, 1.0, v21
	v_mul_f32_e32 v63, v52, v53
	v_fma_f32 v53, v66, v122, v110
	v_rcp_f32_e32 v21, v21
	v_mul_f32_e32 v53, 0xbfb8aa3b, v53
	v_add_f32_e32 v5, 1.0, v5
	v_exp_f32_e32 v53, v53
	v_mul_f32_e32 v45, v36, v37
	v_fma_f32 v37, v46, v122, v110
	v_rcp_f32_e32 v5, v5
	v_mul_f32_e32 v37, 0xbfb8aa3b, v37
	v_exp_f32_e32 v37, v37
	v_mul_f32_e32 v29, v20, v21
	v_fma_f32 v21, v30, v122, v110
	v_mul_f32_e32 v21, 0xbfb8aa3b, v21
	v_add_f32_e32 v53, 1.0, v53
	v_exp_f32_e32 v21, v21
	v_mul_f32_e32 v13, v4, v5
	v_fma_f32 v5, v14, v122, v110
	v_rcp_f32_e32 v53, v53
	v_mul_f32_e32 v5, 0xbfb8aa3b, v5
	v_add_f32_e32 v37, 1.0, v37
	v_exp_f32_e32 v5, v5
	v_rcp_f32_e32 v37, v37
	v_fma_f32 v52, v54, v118, v102
	v_add_f32_e32 v21, 1.0, v21
	v_mul_f32_e32 v54, v52, v53
	v_fma_f32 v53, v67, v123, v111
	v_rcp_f32_e32 v21, v21
	v_mul_f32_e32 v53, 0xbfb8aa3b, v53
	v_fma_f32 v36, v38, v118, v102
	v_add_f32_e32 v5, 1.0, v5
	v_exp_f32_e32 v53, v53
	v_mul_f32_e32 v38, v36, v37
	v_fma_f32 v37, v47, v123, v111
	v_rcp_f32_e32 v5, v5
	v_mul_f32_e32 v37, 0xbfb8aa3b, v37
	v_fma_f32 v20, v22, v118, v102
	v_exp_f32_e32 v37, v37
	v_mul_f32_e32 v22, v20, v21
	v_fma_f32 v21, v31, v123, v111
	v_mul_f32_e32 v21, 0xbfb8aa3b, v21
	v_fma_f32 v4, v6, v118, v102
	v_fmac_f32_e32 v111, v15, v123
	v_add_f32_e32 v53, 1.0, v53
	v_exp_f32_e32 v21, v21
	v_mul_f32_e32 v6, v4, v5
	v_mul_f32_e32 v4, 0xbfb8aa3b, v111
	v_rcp_f32_e32 v53, v53
	v_exp_f32_e32 v4, v4
	v_add_f32_e32 v37, 1.0, v37
	v_rcp_f32_e32 v37, v37
	v_fma_f32 v52, v55, v119, v103
	v_add_f32_e32 v21, 1.0, v21
	v_mul_f32_e32 v55, v52, v53
	v_fma_f32 v52, v56, v96, v84
	v_rcp_f32_e32 v21, v21
	v_add_f32_e32 v4, 1.0, v4
	v_mul_f32_e32 v52, 0xbfb8aa3b, v52
	v_fma_f32 v36, v39, v119, v103
	v_rcp_f32_e32 v4, v4
	v_exp_f32_e32 v52, v52
	v_mul_f32_e32 v39, v36, v37
	v_fma_f32 v36, v40, v96, v84
	v_mul_f32_e32 v36, 0xbfb8aa3b, v36
	v_fma_f32 v20, v23, v119, v103
	v_exp_f32_e32 v36, v36
	v_mul_f32_e32 v23, v20, v21
	v_fma_f32 v20, v24, v96, v84
	v_fmac_f32_e32 v103, v7, v119
	v_mul_f32_e32 v20, 0xbfb8aa3b, v20
	v_mul_f32_e32 v7, v103, v4
	v_fma_f32 v4, v8, v96, v84
	v_add_f32_e32 v52, 1.0, v52
	v_exp_f32_e32 v20, v20
	v_mul_f32_e32 v4, 0xbfb8aa3b, v4
	v_rcp_f32_e32 v52, v52
	v_exp_f32_e32 v4, v4
	v_add_f32_e32 v36, 1.0, v36
	v_rcp_f32_e32 v36, v36
	v_add_f32_e32 v20, 1.0, v20
	v_mul_f32_e32 v56, v48, v52
	v_fma_f32 v48, v49, v89, v77
	v_fma_f32 v49, v57, v97, v85
	v_rcp_f32_e32 v20, v20
	v_add_f32_e32 v4, 1.0, v4
	v_mul_f32_e32 v49, 0xbfb8aa3b, v49
	v_rcp_f32_e32 v4, v4
	v_exp_f32_e32 v49, v49
	v_mul_f32_e32 v40, v32, v36
	v_fma_f32 v32, v33, v89, v77
	v_fma_f32 v33, v41, v97, v85
	v_mul_f32_e32 v33, 0xbfb8aa3b, v33
	v_exp_f32_e32 v33, v33
	v_mul_f32_e32 v24, v16, v20
	v_fma_f32 v16, v17, v89, v77
	v_fma_f32 v17, v25, v97, v85
	v_fma_f32 v0, v0, v88, v76
	v_mul_f32_e32 v17, 0xbfb8aa3b, v17
	v_mul_f32_e32 v8, v0, v4
	v_fma_f32 v0, v1, v89, v77
	v_fma_f32 v1, v9, v97, v85
	v_add_f32_e32 v49, 1.0, v49
	v_exp_f32_e32 v17, v17
	v_mul_f32_e32 v1, 0xbfb8aa3b, v1
	v_rcp_f32_e32 v49, v49
	v_exp_f32_e32 v1, v1
	v_add_f32_e32 v33, 1.0, v33
	v_rcp_f32_e32 v33, v33
	v_add_f32_e32 v17, 1.0, v17
	v_mul_f32_e32 v57, v48, v49
	v_fma_f32 v49, v58, v98, v86
	v_rcp_f32_e32 v17, v17
	v_add_f32_e32 v1, 1.0, v1
	v_mul_f32_e32 v49, 0xbfb8aa3b, v49
	v_rcp_f32_e32 v1, v1
	v_exp_f32_e32 v49, v49
	v_mul_f32_e32 v41, v32, v33
	v_fma_f32 v33, v42, v98, v86
	v_mul_f32_e32 v33, 0xbfb8aa3b, v33
	v_exp_f32_e32 v33, v33
	v_mul_f32_e32 v25, v16, v17
	v_fma_f32 v17, v26, v98, v86
	v_mul_f32_e32 v17, 0xbfb8aa3b, v17
	v_mul_f32_e32 v9, v0, v1
	v_fma_f32 v1, v10, v98, v86
	v_add_f32_e32 v49, 1.0, v49
	v_exp_f32_e32 v17, v17
	v_mul_f32_e32 v1, 0xbfb8aa3b, v1
	v_rcp_f32_e32 v49, v49
	v_exp_f32_e32 v1, v1
	v_add_f32_e32 v33, 1.0, v33
	v_rcp_f32_e32 v33, v33
	v_fma_f32 v48, v50, v90, v78
	v_add_f32_e32 v17, 1.0, v17
	v_mul_f32_e32 v58, v48, v49
	v_fma_f32 v49, v59, v99, v87
	v_rcp_f32_e32 v17, v17
	v_add_f32_e32 v1, 1.0, v1
	v_mul_f32_e32 v49, 0xbfb8aa3b, v49
	v_fma_f32 v32, v34, v90, v78
	v_rcp_f32_e32 v1, v1
	v_exp_f32_e32 v49, v49
	v_mul_f32_e32 v42, v32, v33
	v_fma_f32 v33, v43, v99, v87
	v_mul_f32_e32 v33, 0xbfb8aa3b, v33
	v_fma_f32 v16, v18, v90, v78
	v_exp_f32_e32 v33, v33
	v_mul_f32_e32 v26, v16, v17
	v_fma_f32 v17, v27, v99, v87
	v_fma_f32 v0, v2, v90, v78
	v_fmac_f32_e32 v87, v11, v99
	v_mul_f32_e32 v17, 0xbfb8aa3b, v17
	v_mul_f32_e32 v10, v0, v1
	v_mul_f32_e32 v0, 0xbfb8aa3b, v87
	v_add_f32_e32 v49, 1.0, v49
	v_exp_f32_e32 v17, v17
	v_exp_f32_e32 v0, v0
	v_rcp_f32_e32 v49, v49
	v_add_f32_e32 v33, 1.0, v33
	v_rcp_f32_e32 v33, v33
	v_add_u32_e32 v60, 0x20000, v200
	v_mov_b32_e32 v61, v201
	v_fma_f32 v48, v51, v91, v79
	v_add_f32_e32 v17, 1.0, v17
	v_add_f32_e32 v0, 1.0, v0
	v_mul_f32_e32 v51, v48, v49
	v_lshl_add_u64 v[52:53], v[60:61], 1, s[10:11]
	v_cvt_pk_bf16_f32 v48, v62, v63
	v_cvt_pk_bf16_f32 v49, v54, v55
	v_rcp_f32_e32 v17, v17
	v_rcp_f32_e32 v0, v0
	v_cvt_pk_bf16_f32 v50, v56, v57
	v_cvt_pk_bf16_f32 v51, v58, v51
	global_store_dwordx4 v[52:53], v[48:51], off
	v_fma_f32 v32, v35, v91, v79
	v_mul_f32_e32 v35, v32, v33
	v_add_u32_e32 v48, 0x24000, v200
	v_mov_b32_e32 v49, v201
	v_lshl_add_u64 v[36:37], v[48:49], 1, s[10:11]
	v_cvt_pk_bf16_f32 v32, v44, v45
	v_cvt_pk_bf16_f32 v33, v38, v39
	v_cvt_pk_bf16_f32 v34, v40, v41
	v_cvt_pk_bf16_f32 v35, v42, v35
	global_store_dwordx4 v[36:37], v[32:35], off
	v_fma_f32 v16, v19, v91, v79
	v_fmac_f32_e32 v79, v3, v91
	v_add_u32_e32 v32, 0x28000, v200
	v_mov_b32_e32 v33, v201
	v_mul_f32_e32 v19, v16, v17
	v_lshl_add_u64 v[20:21], v[32:33], 1, s[10:11]
	v_add_u32_e32 v200, 0x2c000, v200
	v_mul_f32_e32 v3, v79, v0
	v_cvt_pk_bf16_f32 v16, v28, v29
	v_cvt_pk_bf16_f32 v17, v22, v23
	v_cvt_pk_bf16_f32 v18, v24, v25
	v_cvt_pk_bf16_f32 v19, v26, v19
	global_store_dwordx4 v[20:21], v[16:19], off
	v_lshl_add_u64 v[4:5], v[200:201], 1, s[10:11]
	v_cvt_pk_bf16_f32 v0, v12, v13
	v_cvt_pk_bf16_f32 v1, v6, v7
	v_cvt_pk_bf16_f32 v2, v8, v9
	v_cvt_pk_bf16_f32 v3, v10, v3
	s_mov_b64 s[10:11], -1
	global_store_dwordx4 v[4:5], v[0:3], off
	s_cbranch_vccnz .LBB0_259
	s_and_b64 vcc, exec, s[4:5]
	v_mov_b64 v[148:149], 0
	v_mov_b64 v[150:151], 0
	v_mov_b64 v[144:145], 0
	v_mov_b64 v[146:147], 0
	v_mov_b64 v[132:133], 0
	v_mov_b64 v[134:135], 0
	v_mov_b64 v[128:129], 0
	v_mov_b64 v[130:131], 0
	v_mov_b64 v[104:105], 0
	v_mov_b64 v[106:107], 0
	v_mov_b64 v[92:93], 0
	v_mov_b64 v[94:95], 0
	v_mov_b64 v[68:69], 0
	v_mov_b64 v[70:71], 0
	v_mov_b64 v[60:61], 0
	v_mov_b64 v[62:63], 0
	v_mov_b64 v[156:157], 0
	v_mov_b64 v[158:159], 0
	v_mov_b64 v[152:153], 0
	v_mov_b64 v[154:155], 0
	v_mov_b64 v[140:141], 0
	v_mov_b64 v[142:143], 0
	v_mov_b64 v[136:137], 0
	v_mov_b64 v[138:139], 0
	v_mov_b64 v[124:125], 0
	v_mov_b64 v[126:127], 0
	v_mov_b64 v[112:113], 0
	v_mov_b64 v[114:115], 0
	v_mov_b64 v[80:81], 0
	v_mov_b64 v[82:83], 0
	v_mov_b64 v[72:73], 0
	v_mov_b64 v[74:75], 0
	v_mov_b64 v[52:53], 0
	v_mov_b64 v[54:55], 0
	v_mov_b64 v[48:49], 0
	v_mov_b64 v[50:51], 0
	v_mov_b64 v[36:37], 0
	v_mov_b64 v[38:39], 0
	v_mov_b64 v[32:33], 0
	v_mov_b64 v[34:35], 0
	v_mov_b64 v[20:21], 0
	v_mov_b64 v[22:23], 0
	v_mov_b64 v[16:17], 0
	v_mov_b64 v[18:19], 0
	v_mov_b64 v[4:5], 0
	v_mov_b64 v[6:7], 0
	v_mov_b64 v[0:1], 0
	v_mov_b64 v[2:3], 0
	v_mov_b64 v[64:65], 0
	v_mov_b64 v[66:67], 0
	v_mov_b64 v[56:57], 0
	v_mov_b64 v[58:59], 0
	v_mov_b64 v[44:45], 0
	v_mov_b64 v[46:47], 0
	v_mov_b64 v[40:41], 0
	v_mov_b64 v[42:43], 0
	v_mov_b64 v[28:29], 0
	v_mov_b64 v[30:31], 0
	v_mov_b64 v[24:25], 0
	v_mov_b64 v[26:27], 0
	v_mov_b64 v[12:13], 0
	v_mov_b64 v[14:15], 0
	v_mov_b64 v[8:9], 0
	v_mov_b64 v[10:11], 0
	s_cbranch_vccnz .LBB0_258
	s_barrier
	s_branch .LBB0_258

.LBB0_278:
	s_lshl_b32 s0, s31, 7
	v_and_b32_e32 v1, 15, v0
	v_and_b32_e32 v2, 48, v0
	v_lshlrev_b32_e32 v0, 2, v0
	s_add_u32 s27, s76, 0x4b400000
	v_lshl_or_b32 v1, v1, 6, v2
	v_and_b32_e32 v0, 32, v0
	s_addc_u32 s33, s77, 0
	v_bitop3_b32 v156, v1, s0, v0 bitop3:0xde
	s_add_u32 s0, s76, 0x200000
	s_addc_u32 s1, s77, 0
	s_bitcmp0_b32 s75, 0
	s_cselect_b64 s[6:7], -1, 0
	s_add_i32 s8, s3, 0x80
	s_add_u32 s8, s25, s8
	s_waitcnt vmcnt(2)
	s_barrier
	s_addc_u32 s9, s26, 0
	s_mov_b32 m0, s44
	s_nop 4
	global_load_lds_dwordx4 v154, s[8:9]
	s_mov_b32 m0, s45
	s_nop 4
	global_load_lds_dwordx4 v155, s[8:9]
	s_add_i32 s8, s18, 0x80
	s_add_u32 s8, s28, s8
	s_addc_u32 s9, s29, 0
	s_mov_b32 m0, s46
	s_nop 4
	global_load_lds_dwordx4 v154, s[8:9]
	s_mov_b32 m0, s47
	s_nop 4
	global_load_lds_dwordx4 v155, s[8:9]
	s_add_i32 s8, s3, 0x20080
	s_add_u32 s8, s25, s8
	s_addc_u32 s9, s26, 0
	s_mov_b32 m0, s48
	s_nop 4
	global_load_lds_dwordx4 v154, s[8:9]
	s_mov_b32 m0, s49
	s_nop 4
	global_load_lds_dwordx4 v155, s[8:9]
	s_waitcnt vmcnt(6)
	s_lshl_b32 s8, s31, 2
	v_bitop3_b32 v128, v1, s22, v0 bitop3:0xde
	s_add_u32 s58, s15, s8
	s_mov_b32 s36, 0
	s_addc_u32 s59, s24, 0
	v_add_u32_e32 v157, s91, v128
	s_mov_b32 s62, s3
	s_mov_b32 s63, s18
	s_barrier
	v_mov_b64 v[120:121], 0
	v_mov_b64 v[122:123], 0
	v_mov_b64 v[124:125], 0
	v_mov_b64 v[126:127], 0
	v_mov_b64 v[112:113], 0
	v_mov_b64 v[114:115], 0
	v_mov_b64 v[116:117], 0
	v_mov_b64 v[118:119], 0
	v_mov_b64 v[104:105], 0
	v_mov_b64 v[106:107], 0
	v_mov_b64 v[108:109], 0
	v_mov_b64 v[110:111], 0
	v_mov_b64 v[88:89], 0
	v_mov_b64 v[90:91], 0
	v_mov_b64 v[92:93], 0
	v_mov_b64 v[94:95], 0
	s_waitcnt vmcnt(0)
	v_mov_b64 v[56:57], 0
	v_mov_b64 v[58:59], 0
	v_mov_b64 v[60:61], 0
	v_mov_b64 v[62:63], 0
	v_mov_b64 v[48:49], 0
	v_mov_b64 v[50:51], 0
	v_mov_b64 v[52:53], 0
	v_mov_b64 v[54:55], 0
	v_mov_b64 v[36:37], 0
	v_mov_b64 v[38:39], 0
	v_mov_b64 v[44:45], 0
	v_mov_b64 v[46:47], 0
	v_mov_b64 v[20:21], 0
	v_mov_b64 v[22:23], 0
	v_mov_b64 v[28:29], 0
	v_mov_b64 v[30:31], 0
	v_mov_b64 v[96:97], 0
	v_mov_b64 v[98:99], 0
	v_mov_b64 v[100:101], 0
	v_mov_b64 v[102:103], 0
	v_mov_b64 v[80:81], 0
	v_mov_b64 v[82:83], 0
	v_mov_b64 v[84:85], 0
	v_mov_b64 v[86:87], 0
	v_mov_b64 v[72:73], 0
	v_mov_b64 v[74:75], 0
	v_mov_b64 v[76:77], 0
	v_mov_b64 v[78:79], 0
	v_mov_b64 v[64:65], 0
	v_mov_b64 v[66:67], 0
	v_mov_b64 v[68:69], 0
	v_mov_b64 v[70:71], 0
	v_mov_b64 v[32:33], 0
	v_mov_b64 v[34:35], 0
	v_mov_b64 v[40:41], 0
	v_mov_b64 v[42:43], 0
	v_mov_b64 v[16:17], 0
	v_mov_b64 v[18:19], 0
	v_mov_b64 v[24:25], 0
	v_mov_b64 v[26:27], 0
	v_mov_b64 v[8:9], 0
	v_mov_b64 v[10:11], 0
	v_mov_b64 v[12:13], 0
	v_mov_b64 v[14:15], 0
	v_mov_b64 v[0:1], 0
	v_mov_b64 v[2:3], 0
	v_mov_b64 v[4:5], 0
	v_mov_b64 v[6:7], 0
	s_branch .LBB0_281

.LBB0_319:
	v_mul_f32_e32 v4, v4, v70
	v_mul_f32_e32 v0, v0, v74
	s_waitcnt vmcnt(0)
	v_mul_f32_e32 v12, v4, v9
	v_mul_f32_e32 v4, v4, v8
	v_fma_f32 v12, v0, v8, -v12
	v_fmac_f32_e32 v4, v0, v9
	v_mul_f32_e32 v0, v1, v60
	v_mul_f32_e32 v1, v5, v71
	v_mul_f32_e32 v5, v1, v11
	v_fma_f32 v5, v0, v10, -v5
	v_mul_f32_e32 v1, v1, v10
	v_mov_b32_e32 v8, v201
	v_fmac_f32_e32 v1, v0, v11
	v_mul_f32_e32 v0, v2, v61
	v_mul_f32_e32 v2, v6, v72
	v_cvt_pk_fp8_f32 v8, v12, v5
	v_mov_b32_e32 v5, v201
	v_mul_f32_e32 v6, v2, v17
	v_mul_f32_e32 v2, v2, v16
	v_cvt_pk_fp8_f32 v5, v4, v1
	v_fma_f32 v6, v0, v16, -v6
	v_fmac_f32_e32 v2, v0, v17
	v_mul_f32_e32 v0, v3, v62
	v_mul_f32_e32 v3, v7, v73
	v_mul_f32_e32 v7, v3, v19
	v_mul_f32_e32 v1, v3, v18
	v_fma_f32 v7, v0, v18, -v7
	v_fmac_f32_e32 v1, v0, v19
	v_cvt_pk_fp8_f32 v8, v6, v7 op_sel:[0,0,1]
	v_cvt_pk_fp8_f32 v5, v2, v1 op_sel:[0,0,1]
	global_store_dword v[82:83], v8, off offset:128
	global_store_dword v[82:83], v5, off offset:144
	s_andn2_b64 vcc, exec, s[8:9]
	s_mov_b64 s[2:3], -1
	s_cbranch_vccnz .LBB0_280
	s_and_b64 vcc, exec, s[4:5]
	v_mov_b64 v[120:121], 0
	v_mov_b64 v[122:123], 0
	v_mov_b64 v[124:125], 0
	v_mov_b64 v[126:127], 0
	v_mov_b64 v[112:113], 0
	v_mov_b64 v[114:115], 0
	v_mov_b64 v[116:117], 0
	v_mov_b64 v[118:119], 0
	v_mov_b64 v[104:105], 0
	v_mov_b64 v[106:107], 0
	v_mov_b64 v[108:109], 0
	v_mov_b64 v[110:111], 0
	v_mov_b64 v[88:89], 0
	v_mov_b64 v[90:91], 0
	v_mov_b64 v[92:93], 0
	v_mov_b64 v[94:95], 0
	v_mov_b64 v[56:57], 0
	v_mov_b64 v[58:59], 0
	v_mov_b64 v[60:61], 0
	v_mov_b64 v[62:63], 0
	v_mov_b64 v[48:49], 0
	v_mov_b64 v[50:51], 0
	v_mov_b64 v[52:53], 0
	v_mov_b64 v[54:55], 0
	v_mov_b64 v[36:37], 0
	v_mov_b64 v[38:39], 0
	v_mov_b64 v[44:45], 0
	v_mov_b64 v[46:47], 0
	v_mov_b64 v[20:21], 0
	v_mov_b64 v[22:23], 0
	v_mov_b64 v[28:29], 0
	v_mov_b64 v[30:31], 0
	v_mov_b64 v[96:97], 0
	v_mov_b64 v[98:99], 0
	v_mov_b64 v[100:101], 0
	v_mov_b64 v[102:103], 0
	v_mov_b64 v[80:81], 0
	v_mov_b64 v[82:83], 0
	v_mov_b64 v[84:85], 0
	v_mov_b64 v[86:87], 0
	v_mov_b64 v[72:73], 0
	v_mov_b64 v[74:75], 0
	v_mov_b64 v[76:77], 0
	v_mov_b64 v[78:79], 0
	v_mov_b64 v[64:65], 0
	v_mov_b64 v[66:67], 0
	v_mov_b64 v[68:69], 0
	v_mov_b64 v[70:71], 0
	v_mov_b64 v[32:33], 0
	v_mov_b64 v[34:35], 0
	v_mov_b64 v[40:41], 0
	v_mov_b64 v[42:43], 0
	v_mov_b64 v[16:17], 0
	v_mov_b64 v[18:19], 0
	v_mov_b64 v[24:25], 0
	v_mov_b64 v[26:27], 0
	v_mov_b64 v[8:9], 0
	v_mov_b64 v[10:11], 0
	v_mov_b64 v[12:13], 0
	v_mov_b64 v[14:15], 0
	v_mov_b64 v[0:1], 0
	v_mov_b64 v[2:3], 0
	v_mov_b64 v[4:5], 0
	v_mov_b64 v[6:7], 0
	s_cbranch_vccnz .LBB0_279
	s_barrier
	s_branch .LBB0_279

.LBB0_326:
	s_lshl_b32 s9, s75, 12
	s_and_b32 s9, s9, 0x3000
	v_and_b32_e32 v1, 15, v0
	v_and_b32_e32 v2, 48, v0
	v_lshlrev_b32_e32 v0, 2, v0
	s_add_u32 s20, s76, 0x53c00000
	v_lshlrev_b32_e32 v1, 6, v1
	v_and_b32_e32 v0, 32, v0
	s_addc_u32 s21, s77, 0
	v_or_b32_e32 v3, v1, v2
	v_bitop3_b32 v1, v1, v0, v2 bitop3:0x36
	s_add_u32 s15, s15, 0x2000
	v_or_b32_e32 v135, s9, v1
	s_addc_u32 s24, s24, 0
	v_readlane_b32 s9, v254, 35
	s_xor_b32 s9, s9, 0x80
	s_lshl_b32 s11, s3, 8
	s_lshr_b32 s9, s9, 6
	s_add_i32 s10, s3, 0xffffff80
	s_and_b32 s11, s11, 0xf00
	s_cmpk_lt_i32 s3, 0x80
	s_cselect_b32 s3, s9, s10
	s_cselect_b32 s9, s11, 0x1000
	s_lshl_b32 s3, s3, 10
	s_or_b32 s3, s3, s2
	s_mulk_i32 s3, 0x1100
	s_or_b32 s3, s3, s9
	s_add_u32 s0, s0, 0x80
	s_addc_u32 s1, s1, 0
	s_waitcnt vmcnt(2)
	s_barrier
	s_mov_b32 m0, s44
	s_nop 4
	global_load_lds_dwordx4 v132, s[0:1]
	s_add_u32 s6, s6, 0x80
	s_mov_b32 m0, s45
	s_nop 4
	global_load_lds_dwordx4 v134, s[0:1]
	s_addc_u32 s7, s7, 0
	s_or_b32 s9, s8, 0x20080
	s_mov_b32 m0, s46
	s_nop 4
	global_load_lds_dwordx4 v131, s[6:7]
	s_add_u32 s10, s28, s9
	s_mov_b32 m0, s47
	s_nop 4
	global_load_lds_dwordx4 v133, s[6:7]
	s_addc_u32 s11, s29, 0
	s_and_b32 s9, s14, 64
	s_lshr_b32 s14, s14, 1
	s_mov_b32 m0, s48
	s_nop 4
	global_load_lds_dwordx4 v132, s[10:11]
	s_and_b32 s14, s14, 16
	s_mov_b32 m0, s49
	s_nop 4
	global_load_lds_dwordx4 v134, s[10:11]
	s_or_b32 s14, s14, s9
	s_waitcnt vmcnt(6)
	v_bitop3_b32 v128, v3, s22, v0 bitop3:0xde
	s_add_u32 s25, s18, 0x20080
	s_addc_u32 s26, s19, 0
	s_mov_b32 s27, 0
	v_add_u32_e32 v136, s91, v128
	s_mov_b32 s58, s8
	s_barrier
	v_mov_b64 v[112:113], 0
	v_mov_b64 v[114:115], 0
	v_mov_b64 v[116:117], 0
	v_mov_b64 v[118:119], 0
	v_mov_b64 v[96:97], 0
	v_mov_b64 v[98:99], 0
	v_mov_b64 v[100:101], 0
	v_mov_b64 v[102:103], 0
	v_mov_b64 v[80:81], 0
	v_mov_b64 v[82:83], 0
	v_mov_b64 v[84:85], 0
	v_mov_b64 v[86:87], 0
	s_waitcnt vmcnt(0)
	v_mov_b64 v[56:57], 0
	v_mov_b64 v[58:59], 0
	v_mov_b64 v[60:61], 0
	v_mov_b64 v[62:63], 0
	v_mov_b64 v[120:121], 0
	v_mov_b64 v[122:123], 0
	v_mov_b64 v[124:125], 0
	v_mov_b64 v[126:127], 0
	v_mov_b64 v[104:105], 0
	v_mov_b64 v[106:107], 0
	v_mov_b64 v[108:109], 0
	v_mov_b64 v[110:111], 0
	v_mov_b64 v[88:89], 0
	v_mov_b64 v[90:91], 0
	v_mov_b64 v[92:93], 0
	v_mov_b64 v[94:95], 0
	v_mov_b64 v[72:73], 0
	v_mov_b64 v[74:75], 0
	v_mov_b64 v[76:77], 0
	v_mov_b64 v[78:79], 0
	v_mov_b64 v[48:49], 0
	v_mov_b64 v[50:51], 0
	v_mov_b64 v[52:53], 0
	v_mov_b64 v[54:55], 0
	v_mov_b64 v[32:33], 0
	v_mov_b64 v[34:35], 0
	v_mov_b64 v[36:37], 0
	v_mov_b64 v[38:39], 0
	v_mov_b64 v[16:17], 0
	v_mov_b64 v[18:19], 0
	v_mov_b64 v[20:21], 0
	v_mov_b64 v[22:23], 0
	v_mov_b64 v[0:1], 0
	v_mov_b64 v[2:3], 0
	v_mov_b64 v[4:5], 0
	v_mov_b64 v[6:7], 0
	v_mov_b64 v[64:65], 0
	v_mov_b64 v[66:67], 0
	v_mov_b64 v[68:69], 0
	v_mov_b64 v[70:71], 0
	v_mov_b64 v[40:41], 0
	v_mov_b64 v[42:43], 0
	v_mov_b64 v[44:45], 0
	v_mov_b64 v[46:47], 0
	v_mov_b64 v[24:25], 0
	v_mov_b64 v[26:27], 0
	v_mov_b64 v[28:29], 0
	v_mov_b64 v[30:31], 0
	v_mov_b64 v[8:9], 0
	v_mov_b64 v[10:11], 0
	v_mov_b64 v[12:13], 0
	v_mov_b64 v[14:15], 0
	s_branch .LBB0_329

.LBB0_335:
	s_add_u32 s0, s20, s3
	s_addc_u32 s1, s21, 0
	s_ashr_i32 s3, s2, 31
	s_lshl_b64 s[2:3], s[2:3], 2
	v_mbcnt_lo_u32_b32 v128, -1, 0
	v_mbcnt_hi_u32_b32 v128, -1, v128
	s_add_u32 s2, s15, s2
	v_and_or_b32 v138, v128, 15, s55
	s_addc_u32 s3, s24, s3
	v_lshrrev_b32_e32 v129, 2, v128
	v_ashrrev_i32_e32 v139, 31, v138
	v_and_b32_e32 v137, 12, v129
	v_lshl_add_u64 v[128:129], v[138:139], 2, s[2:3]
	global_load_dword v140, v[128:129], off
	s_movk_i32 s2, 0x1100
	v_mul_lo_u32 v138, v138, s2
	v_or3_b32 v137, s14, v137, v138
	v_mov_b32_e32 v138, v201
	s_waitcnt vmcnt(0)
	v_pk_mul_f32 v[112:113], v[112:113], v[140:141] op_sel_hi:[1,0]
	v_pk_mul_f32 v[116:117], v[116:117], v[140:141] op_sel_hi:[1,0]
	v_cvt_pk_fp8_f32 v138, v112, v113
	v_mov_b32_e32 v112, v201
	v_cvt_pk_fp8_f32 v112, v116, v117
	v_pk_mul_f32 v[114:115], v[114:115], v[140:141] op_sel_hi:[1,0]
	v_pk_mul_f32 v[118:119], v[118:119], v[140:141] op_sel_hi:[1,0]
	v_cvt_pk_fp8_f32 v138, v114, v115 op_sel:[0,0,1]
	v_cvt_pk_fp8_f32 v112, v118, v119 op_sel:[0,0,1]
	v_pk_mul_f32 v[114:115], v[120:121], v[140:141] op_sel_hi:[1,0]
	v_mov_b32_e32 v120, v201
	v_cvt_pk_fp8_f32 v120, v114, v115
	global_store_dword v137, v112, s[0:1] offset:32
	v_pk_mul_f32 v[112:113], v[122:123], v[140:141] op_sel_hi:[1,0]
	v_pk_mul_f32 v[118:119], v[124:125], v[140:141] op_sel_hi:[1,0]
	v_cvt_pk_fp8_f32 v120, v112, v113 op_sel:[0,0,1]
	v_mov_b32_e32 v112, v201
	v_cvt_pk_fp8_f32 v112, v118, v119
	v_pk_mul_f32 v[116:117], v[126:127], v[140:141] op_sel_hi:[1,0]
	global_store_dword v137, v138, s[0:1]
	global_store_dword v137, v120, s[0:1] offset:128
	v_cvt_pk_fp8_f32 v112, v116, v117 op_sel:[0,0,1]
	global_store_dword v137, v112, s[0:1] offset:160
	global_load_dword v112, v[128:129], off offset:64
	v_add_u32_e32 v113, 0x11000, v137
	v_mov_b32_e32 v114, v201
	s_waitcnt vmcnt(0)
	v_pk_mul_f32 v[96:97], v[96:97], v[112:113] op_sel_hi:[1,0]
	v_pk_mul_f32 v[100:101], v[100:101], v[112:113] op_sel_hi:[1,0]
	v_cvt_pk_fp8_f32 v114, v96, v97
	v_mov_b32_e32 v96, v201
	v_cvt_pk_fp8_f32 v96, v100, v101
	v_pk_mul_f32 v[98:99], v[98:99], v[112:113] op_sel_hi:[1,0]
	v_pk_mul_f32 v[102:103], v[102:103], v[112:113] op_sel_hi:[1,0]
	v_cvt_pk_fp8_f32 v114, v98, v99 op_sel:[0,0,1]
	v_cvt_pk_fp8_f32 v96, v102, v103 op_sel:[0,0,1]
	v_pk_mul_f32 v[98:99], v[104:105], v[112:113] op_sel_hi:[1,0]
	v_mov_b32_e32 v104, v201
	v_cvt_pk_fp8_f32 v104, v98, v99
	global_store_dword v113, v96, s[0:1] offset:32
	v_pk_mul_f32 v[96:97], v[106:107], v[112:113] op_sel_hi:[1,0]
	v_pk_mul_f32 v[102:103], v[108:109], v[112:113] op_sel_hi:[1,0]
	v_cvt_pk_fp8_f32 v104, v96, v97 op_sel:[0,0,1]
	v_mov_b32_e32 v96, v201
	v_cvt_pk_fp8_f32 v96, v102, v103
	v_pk_mul_f32 v[100:101], v[110:111], v[112:113] op_sel_hi:[1,0]
	global_store_dword v113, v114, s[0:1]
	global_store_dword v113, v104, s[0:1] offset:128
	v_cvt_pk_fp8_f32 v96, v100, v101 op_sel:[0,0,1]
	global_store_dword v113, v96, s[0:1] offset:160
	global_load_dword v96, v[128:129], off offset:128
	v_add_u32_e32 v97, 0x22000, v137
	v_mov_b32_e32 v98, v201
	s_waitcnt vmcnt(0)
	v_pk_mul_f32 v[80:81], v[80:81], v[96:97] op_sel_hi:[1,0]
	v_pk_mul_f32 v[84:85], v[84:85], v[96:97] op_sel_hi:[1,0]
	v_cvt_pk_fp8_f32 v98, v80, v81
	v_mov_b32_e32 v80, v201
	v_cvt_pk_fp8_f32 v80, v84, v85
	v_pk_mul_f32 v[82:83], v[82:83], v[96:97] op_sel_hi:[1,0]
	v_pk_mul_f32 v[86:87], v[86:87], v[96:97] op_sel_hi:[1,0]
	v_cvt_pk_fp8_f32 v98, v82, v83 op_sel:[0,0,1]
	v_cvt_pk_fp8_f32 v80, v86, v87 op_sel:[0,0,1]
	v_pk_mul_f32 v[82:83], v[88:89], v[96:97] op_sel_hi:[1,0]
	v_mov_b32_e32 v88, v201
	v_cvt_pk_fp8_f32 v88, v82, v83
	global_store_dword v97, v80, s[0:1] offset:32
	v_pk_mul_f32 v[80:81], v[90:91], v[96:97] op_sel_hi:[1,0]
	v_pk_mul_f32 v[86:87], v[92:93], v[96:97] op_sel_hi:[1,0]
	v_cvt_pk_fp8_f32 v88, v80, v81 op_sel:[0,0,1]
	v_mov_b32_e32 v80, v201
	v_cvt_pk_fp8_f32 v80, v86, v87
	v_pk_mul_f32 v[84:85], v[94:95], v[96:97] op_sel_hi:[1,0]
	global_store_dword v97, v98, s[0:1]
	global_store_dword v97, v88, s[0:1] offset:128
	v_cvt_pk_fp8_f32 v80, v84, v85 op_sel:[0,0,1]
	global_store_dword v97, v80, s[0:1] offset:160
	global_load_dword v80, v[128:129], off offset:192
	v_add_u32_e32 v81, 0x33000, v137
	v_mov_b32_e32 v82, v201
	s_waitcnt vmcnt(0)
	v_pk_mul_f32 v[56:57], v[56:57], v[80:81] op_sel_hi:[1,0]
	v_pk_mul_f32 v[60:61], v[60:61], v[80:81] op_sel_hi:[1,0]
	v_cvt_pk_fp8_f32 v82, v56, v57
	v_mov_b32_e32 v56, v201
	v_cvt_pk_fp8_f32 v56, v60, v61
	v_pk_mul_f32 v[58:59], v[58:59], v[80:81] op_sel_hi:[1,0]
	v_pk_mul_f32 v[62:63], v[62:63], v[80:81] op_sel_hi:[1,0]
	v_cvt_pk_fp8_f32 v82, v58, v59 op_sel:[0,0,1]
	v_cvt_pk_fp8_f32 v56, v62, v63 op_sel:[0,0,1]
	v_pk_mul_f32 v[58:59], v[72:73], v[80:81] op_sel_hi:[1,0]
	v_mov_b32_e32 v72, v201
	v_cvt_pk_fp8_f32 v72, v58, v59
	global_store_dword v81, v56, s[0:1] offset:32
	v_pk_mul_f32 v[56:57], v[74:75], v[80:81] op_sel_hi:[1,0]
	v_pk_mul_f32 v[62:63], v[76:77], v[80:81] op_sel_hi:[1,0]
	v_cvt_pk_fp8_f32 v72, v56, v57 op_sel:[0,0,1]
	v_mov_b32_e32 v56, v201
	v_cvt_pk_fp8_f32 v56, v62, v63
	v_pk_mul_f32 v[60:61], v[78:79], v[80:81] op_sel_hi:[1,0]
	global_store_dword v81, v82, s[0:1]
	global_store_dword v81, v72, s[0:1] offset:128
	v_cvt_pk_fp8_f32 v56, v60, v61 op_sel:[0,0,1]
	global_store_dword v81, v56, s[0:1] offset:160
	global_load_dword v56, v[128:129], off offset:512
	v_add_u32_e32 v57, 0x88000, v137
	v_mov_b32_e32 v58, v201
	s_waitcnt vmcnt(0)
	v_pk_mul_f32 v[48:49], v[48:49], v[56:57] op_sel_hi:[1,0]
	v_pk_mul_f32 v[52:53], v[52:53], v[56:57] op_sel_hi:[1,0]
	v_cvt_pk_fp8_f32 v58, v48, v49
	v_mov_b32_e32 v48, v201
	v_cvt_pk_fp8_f32 v48, v52, v53
	v_pk_mul_f32 v[54:55], v[54:55], v[56:57] op_sel_hi:[1,0]
	v_pk_mul_f32 v[50:51], v[50:51], v[56:57] op_sel_hi:[1,0]
	v_pk_mul_f32 v[52:53], v[70:71], v[56:57] op_sel_hi:[1,0]
	v_cvt_pk_fp8_f32 v48, v54, v55 op_sel:[0,0,1]
	v_cvt_pk_fp8_f32 v58, v50, v51 op_sel:[0,0,1]
	v_pk_mul_f32 v[50:51], v[64:65], v[56:57] op_sel_hi:[1,0]
	v_pk_mul_f32 v[54:55], v[68:69], v[56:57] op_sel_hi:[1,0]
	global_store_dword v57, v48, s[0:1] offset:32
	v_pk_mul_f32 v[48:49], v[66:67], v[56:57] op_sel_hi:[1,0]
	v_mov_b32_e32 v56, v201
	v_cvt_pk_fp8_f32 v56, v50, v51
	global_store_dword v57, v58, s[0:1]
	v_cvt_pk_fp8_f32 v56, v48, v49 op_sel:[0,0,1]
	v_mov_b32_e32 v48, v201
	v_cvt_pk_fp8_f32 v48, v54, v55
	global_store_dword v57, v56, s[0:1] offset:128
	v_cvt_pk_fp8_f32 v48, v52, v53 op_sel:[0,0,1]
	global_store_dword v57, v48, s[0:1] offset:160
	global_load_dword v48, v[128:129], off offset:576
	v_add_u32_e32 v49, 0x99000, v137
	v_mov_b32_e32 v50, v201
	s_waitcnt vmcnt(0)
	v_pk_mul_f32 v[32:33], v[32:33], v[48:49] op_sel_hi:[1,0]
	v_pk_mul_f32 v[36:37], v[36:37], v[48:49] op_sel_hi:[1,0]
	v_cvt_pk_fp8_f32 v50, v32, v33
	v_mov_b32_e32 v32, v201
	v_cvt_pk_fp8_f32 v32, v36, v37
	v_pk_mul_f32 v[34:35], v[34:35], v[48:49] op_sel_hi:[1,0]
	v_pk_mul_f32 v[38:39], v[38:39], v[48:49] op_sel_hi:[1,0]
	v_cvt_pk_fp8_f32 v50, v34, v35 op_sel:[0,0,1]
	v_cvt_pk_fp8_f32 v32, v38, v39 op_sel:[0,0,1]
	v_pk_mul_f32 v[34:35], v[40:41], v[48:49] op_sel_hi:[1,0]
	v_mov_b32_e32 v40, v201
	v_cvt_pk_fp8_f32 v40, v34, v35
	global_store_dword v49, v32, s[0:1] offset:32
	v_pk_mul_f32 v[32:33], v[42:43], v[48:49] op_sel_hi:[1,0]
	v_pk_mul_f32 v[38:39], v[44:45], v[48:49] op_sel_hi:[1,0]
	v_cvt_pk_fp8_f32 v40, v32, v33 op_sel:[0,0,1]
	v_mov_b32_e32 v32, v201
	v_cvt_pk_fp8_f32 v32, v38, v39
	v_pk_mul_f32 v[36:37], v[46:47], v[48:49] op_sel_hi:[1,0]
	global_store_dword v49, v50, s[0:1]
	global_store_dword v49, v40, s[0:1] offset:128
	v_cvt_pk_fp8_f32 v32, v36, v37 op_sel:[0,0,1]
	global_store_dword v49, v32, s[0:1] offset:160
	global_load_dword v32, v[128:129], off offset:640
	v_add_u32_e32 v33, 0xaa000, v137
	v_mov_b32_e32 v34, v201
	s_waitcnt vmcnt(0)
	v_pk_mul_f32 v[16:17], v[16:17], v[32:33] op_sel_hi:[1,0]
	v_pk_mul_f32 v[20:21], v[20:21], v[32:33] op_sel_hi:[1,0]
	v_cvt_pk_fp8_f32 v34, v16, v17
	v_mov_b32_e32 v16, v201
	v_cvt_pk_fp8_f32 v16, v20, v21
	v_pk_mul_f32 v[18:19], v[18:19], v[32:33] op_sel_hi:[1,0]
	v_pk_mul_f32 v[22:23], v[22:23], v[32:33] op_sel_hi:[1,0]
	v_cvt_pk_fp8_f32 v34, v18, v19 op_sel:[0,0,1]
	v_cvt_pk_fp8_f32 v16, v22, v23 op_sel:[0,0,1]
	v_pk_mul_f32 v[18:19], v[24:25], v[32:33] op_sel_hi:[1,0]
	v_mov_b32_e32 v24, v201
	v_cvt_pk_fp8_f32 v24, v18, v19
	global_store_dword v33, v16, s[0:1] offset:32
	v_pk_mul_f32 v[16:17], v[26:27], v[32:33] op_sel_hi:[1,0]
	v_pk_mul_f32 v[22:23], v[28:29], v[32:33] op_sel_hi:[1,0]
	v_cvt_pk_fp8_f32 v24, v16, v17 op_sel:[0,0,1]
	v_mov_b32_e32 v16, v201
	v_cvt_pk_fp8_f32 v16, v22, v23
	v_pk_mul_f32 v[20:21], v[30:31], v[32:33] op_sel_hi:[1,0]
	global_store_dword v33, v34, s[0:1]
	global_store_dword v33, v24, s[0:1] offset:128
	v_cvt_pk_fp8_f32 v16, v20, v21 op_sel:[0,0,1]
	global_store_dword v33, v16, s[0:1] offset:160
	global_load_dword v16, v[128:129], off offset:704
	v_add_u32_e32 v17, 0xbb000, v137
	v_mov_b32_e32 v18, v201
	s_waitcnt vmcnt(0)
	v_pk_mul_f32 v[0:1], v[0:1], v[16:17] op_sel_hi:[1,0]
	v_pk_mul_f32 v[4:5], v[4:5], v[16:17] op_sel_hi:[1,0]
	v_cvt_pk_fp8_f32 v18, v0, v1
	v_mov_b32_e32 v0, v201
	v_cvt_pk_fp8_f32 v0, v4, v5
	v_pk_mul_f32 v[2:3], v[2:3], v[16:17] op_sel_hi:[1,0]
	v_pk_mul_f32 v[6:7], v[6:7], v[16:17] op_sel_hi:[1,0]
	v_cvt_pk_fp8_f32 v18, v2, v3 op_sel:[0,0,1]
	v_cvt_pk_fp8_f32 v0, v6, v7 op_sel:[0,0,1]
	v_pk_mul_f32 v[2:3], v[8:9], v[16:17] op_sel_hi:[1,0]
	v_mov_b32_e32 v8, v201
	v_cvt_pk_fp8_f32 v8, v2, v3
	global_store_dword v17, v0, s[0:1] offset:32
	v_pk_mul_f32 v[0:1], v[10:11], v[16:17] op_sel_hi:[1,0]
	v_pk_mul_f32 v[6:7], v[12:13], v[16:17] op_sel_hi:[1,0]
	v_cvt_pk_fp8_f32 v8, v0, v1 op_sel:[0,0,1]
	v_mov_b32_e32 v0, v201
	v_cvt_pk_fp8_f32 v0, v6, v7
	v_pk_mul_f32 v[4:5], v[14:15], v[16:17] op_sel_hi:[1,0]
	global_store_dword v17, v18, s[0:1]
	global_store_dword v17, v8, s[0:1] offset:128
	v_cvt_pk_fp8_f32 v0, v4, v5 op_sel:[0,0,1]
	global_store_dword v17, v0, s[0:1] offset:160
	s_andn2_b64 vcc, exec, s[6:7]
	s_mov_b64 s[0:1], -1
	v_mov_b32_e32 v250, v199
	s_cbranch_vccnz .LBB0_328
	s_and_b64 vcc, exec, s[4:5]
	v_mov_b64 v[112:113], 0
	v_mov_b64 v[114:115], 0
	v_mov_b64 v[116:117], 0
	v_mov_b64 v[118:119], 0
	v_mov_b64 v[96:97], 0
	v_mov_b64 v[98:99], 0
	v_mov_b64 v[100:101], 0
	v_mov_b64 v[102:103], 0
	v_mov_b64 v[80:81], 0
	v_mov_b64 v[82:83], 0
	v_mov_b64 v[84:85], 0
	v_mov_b64 v[86:87], 0
	v_mov_b64 v[56:57], 0
	v_mov_b64 v[58:59], 0
	v_mov_b64 v[60:61], 0
	v_mov_b64 v[62:63], 0
	v_mov_b64 v[120:121], 0
	v_mov_b64 v[122:123], 0
	v_mov_b64 v[124:125], 0
	v_mov_b64 v[126:127], 0
	v_mov_b64 v[104:105], 0
	v_mov_b64 v[106:107], 0
	v_mov_b64 v[108:109], 0
	v_mov_b64 v[110:111], 0
	v_mov_b64 v[88:89], 0
	v_mov_b64 v[90:91], 0
	v_mov_b64 v[92:93], 0
	v_mov_b64 v[94:95], 0
	v_mov_b64 v[72:73], 0
	v_mov_b64 v[74:75], 0
	v_mov_b64 v[76:77], 0
	v_mov_b64 v[78:79], 0
	v_mov_b64 v[48:49], 0
	v_mov_b64 v[50:51], 0
	v_mov_b64 v[52:53], 0
	v_mov_b64 v[54:55], 0
	v_mov_b64 v[32:33], 0
	v_mov_b64 v[34:35], 0
	v_mov_b64 v[36:37], 0
	v_mov_b64 v[38:39], 0
	v_mov_b64 v[16:17], 0
	v_mov_b64 v[18:19], 0
	v_mov_b64 v[20:21], 0
	v_mov_b64 v[22:23], 0
	v_mov_b64 v[0:1], 0
	v_mov_b64 v[2:3], 0
	v_mov_b64 v[4:5], 0
	v_mov_b64 v[6:7], 0
	v_mov_b64 v[64:65], 0
	v_mov_b64 v[66:67], 0
	v_mov_b64 v[68:69], 0
	v_mov_b64 v[70:71], 0
	v_mov_b64 v[40:41], 0
	v_mov_b64 v[42:43], 0
	v_mov_b64 v[44:45], 0
	v_mov_b64 v[46:47], 0
	v_mov_b64 v[24:25], 0
	v_mov_b64 v[26:27], 0
	v_mov_b64 v[28:29], 0
	v_mov_b64 v[30:31], 0
	v_mov_b64 v[8:9], 0
	v_mov_b64 v[10:11], 0
	v_mov_b64 v[12:13], 0
	v_mov_b64 v[14:15], 0
	s_cbranch_vccnz .LBB0_327
	s_barrier
	s_branch .LBB0_327

.LBB0_580:
	s_lshl_b32 s5, s5, 10
	s_or_b32 s46, s5, s4
	v_readlane_b32 s4, v254, 43
	s_and_b32 s22, s4, 0x60
	s_lshl_b32 s4, s22, 7
	s_lshl_b32 s5, s9, 13
	v_and_b32_e32 v1, 15, v0
	v_and_b32_e32 v2, 48, v0
	v_lshlrev_b32_e32 v0, 2, v0
	s_add_i32 s23, s79, 0x18000
	s_add_i32 s24, s79, 0x1a000
	s_add_i32 s25, s79, 0x1c000
	s_add_i32 s26, s79, 0x1e000
	s_add_i32 s27, s91, 0x10000
	s_add_i32 s28, s91, 0x14000
	s_add_i32 s29, s79, 0xc000
	s_add_i32 s30, s91, 0x18000
	s_add_i32 s31, s91, 0x1c000
	v_lshl_or_b32 v1, v1, 6, v2
	v_and_b32_e32 v0, 32, v0
	s_cmp_lt_u32 s75, 4
	v_readlane_b32 s9, v254, 45
	v_bitop3_b32 v134, v1, s5, v0 bitop3:0xde
	v_bitop3_b32 v133, v1, s4, v0 bitop3:0xde
	s_cselect_b64 s[4:5], -1, 0
	s_and_b32 s33, s9, 0x3fffc0
	v_readlane_b32 s9, v254, 34
	v_readlane_b32 s10, v254, 35
	s_add_i32 s34, s79, 0xe000
	s_ashr_i32 s35, s9, 31
	s_ashr_i32 s36, s10, 31
	s_ashr_i32 s38, s9, 3
	s_or_b32 s39, s8, 0x1c0
	s_add_i32 s8, s47, 0x80
	s_add_u32 s8, s16, s8
	s_waitcnt vmcnt(2)
	s_barrier
	s_addc_u32 s9, s17, 0
	s_mov_b32 m0, s23
	s_nop 4
	global_load_lds_dwordx4 v130, s[8:9]
	s_mov_b32 m0, s24
	s_nop 4
	global_load_lds_dwordx4 v132, s[8:9]
	s_add_u32 s6, s6, 0x80
	s_addc_u32 s7, s7, 0
	s_mov_b32 m0, s83
	s_nop 4
	global_load_lds_dwordx4 v129, s[6:7]
	s_mov_b32 m0, s84
	s_nop 4
	global_load_lds_dwordx4 v131, s[6:7]
	s_add_i32 s6, s47, 0x100080
	s_add_u32 s6, s16, s6
	s_addc_u32 s7, s17, 0
	s_mov_b32 m0, s25
	s_nop 4
	global_load_lds_dwordx4 v130, s[6:7]
	s_mov_b32 m0, s26
	s_nop 4
	global_load_lds_dwordx4 v132, s[6:7]
	s_waitcnt vmcnt(6)
	s_mov_b32 s40, 0
	v_add_u32_e32 v134, s91, v134
	s_barrier
	v_mov_b64 v[112:113], 0
	v_mov_b64 v[114:115], 0
	v_mov_b64 v[116:117], 0
	v_mov_b64 v[118:119], 0
	v_mov_b64 v[96:97], 0
	v_mov_b64 v[98:99], 0
	v_mov_b64 v[100:101], 0
	v_mov_b64 v[102:103], 0
	s_waitcnt vmcnt(4)
	v_mov_b64 v[72:73], 0
	v_mov_b64 v[74:75], 0
	v_mov_b64 v[76:77], 0
	v_mov_b64 v[78:79], 0
	s_waitcnt vmcnt(11)
	v_mov_b64 v[40:41], 0
	s_waitcnt vmcnt(10)
	v_mov_b64 v[42:43], 0
	s_waitcnt vmcnt(9)
	v_mov_b64 v[44:45], 0
	s_waitcnt vmcnt(8)
	v_mov_b64 v[46:47], 0
	v_mov_b64 v[120:121], 0
	v_mov_b64 v[122:123], 0
	v_mov_b64 v[124:125], 0
	v_mov_b64 v[126:127], 0
	v_mov_b64 v[104:105], 0
	v_mov_b64 v[106:107], 0
	v_mov_b64 v[108:109], 0
	v_mov_b64 v[110:111], 0
	v_mov_b64 v[88:89], 0
	v_mov_b64 v[90:91], 0
	v_mov_b64 v[92:93], 0
	v_mov_b64 v[94:95], 0
	v_mov_b64 v[64:65], 0
	v_mov_b64 v[66:67], 0
	v_mov_b64 v[68:69], 0
	v_mov_b64 v[70:71], 0
	s_waitcnt vmcnt(0)
	v_mov_b64 v[56:57], 0
	s_waitcnt vmcnt(2)
	v_mov_b64 v[58:59], 0
	s_waitcnt vmcnt(1)
	v_mov_b64 v[60:61], 0
	s_waitcnt vmcnt(0)
	v_mov_b64 v[62:63], 0
	v_mov_b64 v[32:33], 0
	v_mov_b64 v[34:35], 0
	v_mov_b64 v[36:37], 0
	v_mov_b64 v[38:39], 0
	v_mov_b64 v[16:17], 0
	v_mov_b64 v[18:19], 0
	v_mov_b64 v[20:21], 0
	v_mov_b64 v[22:23], 0
	v_mov_b64 v[0:1], 0
	v_mov_b64 v[2:3], 0
	v_mov_b64 v[4:5], 0
	v_mov_b64 v[6:7], 0
	v_mov_b64 v[80:81], 0
	v_mov_b64 v[82:83], 0
	v_mov_b64 v[84:85], 0
	v_mov_b64 v[86:87], 0
	v_mov_b64 v[48:49], 0
	v_mov_b64 v[50:51], 0
	v_mov_b64 v[52:53], 0
	v_mov_b64 v[54:55], 0
	v_mov_b64 v[24:25], 0
	v_mov_b64 v[26:27], 0
	v_mov_b64 v[28:29], 0
	v_mov_b64 v[30:31], 0
	v_mov_b64 v[8:9], 0
	v_mov_b64 v[10:11], 0
	v_mov_b64 v[12:13], 0
	v_mov_b64 v[14:15], 0
	s_branch .LBB0_583

.LBB0_603:
	v_mbcnt_lo_u32_b32 v135, -1, 0
	v_mbcnt_hi_u32_b32 v135, -1, v135
	s_mov_b32 s10, 0x3c800000
	v_lshrrev_b32_e32 v136, 1, v135
	v_and_or_b32 v135, v135, 15, s33
	v_and_b32_e32 v136, 24, v136
	v_lshlrev_b32_e32 v135, 10, v135
	v_or3_b32 v135, v136, s22, v135
	v_pk_mul_f32 v[112:113], v[112:113], s[10:11] op_sel_hi:[1,0]
	v_mov_b32_e32 v136, v201
	v_cvt_pk_fp8_f32 v136, v112, v113
	v_pk_mul_f32 v[114:115], v[114:115], s[10:11] op_sel_hi:[1,0]
	v_pk_mul_f32 v[112:113], v[122:123], s[10:11] op_sel_hi:[1,0]
	v_pk_mul_f32 v[96:97], v[96:97], s[10:11] op_sel_hi:[1,0]
	v_cvt_pk_fp8_f32 v136, v114, v115 op_sel:[0,0,1]
	v_pk_mul_f32 v[114:115], v[120:121], s[10:11] op_sel_hi:[1,0]
	v_mov_b32_e32 v120, v201
	v_cvt_pk_fp8_f32 v120, v114, v115
	v_pk_mul_f32 v[98:99], v[98:99], s[10:11] op_sel_hi:[1,0]
	v_pk_mul_f32 v[72:73], v[72:73], s[10:11] op_sel_hi:[1,0]
	v_pk_mul_f32 v[74:75], v[74:75], s[10:11] op_sel_hi:[1,0]
	v_cvt_pk_fp8_f32 v120, v112, v113 op_sel:[0,0,1]
	v_mov_b32_e32 v112, v201
	v_cvt_pk_fp8_f32 v112, v96, v97
	v_pk_mul_f32 v[96:97], v[106:107], s[10:11] op_sel_hi:[1,0]
	v_pk_mul_f32 v[40:41], v[40:41], s[10:11] op_sel_hi:[1,0]
	v_pk_mul_f32 v[44:45], v[44:45], s[10:11] op_sel_hi:[1,0]
	v_cvt_pk_fp8_f32 v112, v98, v99 op_sel:[0,0,1]
	v_pk_mul_f32 v[98:99], v[104:105], s[10:11] op_sel_hi:[1,0]
	v_mov_b32_e32 v104, v201
	v_cvt_pk_fp8_f32 v104, v98, v99
	v_pk_mul_f32 v[116:117], v[116:117], s[10:11] op_sel_hi:[1,0]
	v_mov_b32_e32 v137, v201
	v_pk_mul_f32 v[100:101], v[100:101], s[10:11] op_sel_hi:[1,0]
	v_cvt_pk_fp8_f32 v104, v96, v97 op_sel:[0,0,1]
	v_mov_b32_e32 v96, v201
	v_cvt_pk_fp8_f32 v96, v72, v73
	v_pk_mul_f32 v[72:73], v[90:91], s[10:11] op_sel_hi:[1,0]
	v_mov_b32_e32 v113, v201
	v_pk_mul_f32 v[76:77], v[76:77], s[10:11] op_sel_hi:[1,0]
	v_cvt_pk_fp8_f32 v96, v74, v75 op_sel:[0,0,1]
	v_pk_mul_f32 v[74:75], v[88:89], s[10:11] op_sel_hi:[1,0]
	v_mov_b32_e32 v88, v201
	v_cvt_pk_fp8_f32 v88, v74, v75
	v_mov_b32_e32 v97, v201
	v_cvt_pk_fp8_f32 v137, v116, v117
	v_cvt_pk_fp8_f32 v113, v100, v101
	v_cvt_pk_fp8_f32 v88, v72, v73 op_sel:[0,0,1]
	v_mov_b32_e32 v72, v201
	v_mov_b32_e32 v73, v201
	v_cvt_pk_fp8_f32 v72, v40, v41
	v_cvt_pk_fp8_f32 v73, v44, v45
	v_cvt_pk_fp8_f32 v97, v76, v77
	v_pk_mul_f32 v[42:43], v[42:43], s[10:11] op_sel_hi:[1,0]
	v_pk_mul_f32 v[46:47], v[46:47], s[10:11] op_sel_hi:[1,0]
	v_pk_mul_f32 v[118:119], v[118:119], s[10:11] op_sel_hi:[1,0]
	v_pk_mul_f32 v[102:103], v[102:103], s[10:11] op_sel_hi:[1,0]
	v_pk_mul_f32 v[78:79], v[78:79], s[10:11] op_sel_hi:[1,0]
	v_cvt_pk_fp8_f32 v72, v42, v43 op_sel:[0,0,1]
	v_cvt_pk_fp8_f32 v73, v46, v47 op_sel:[0,0,1]
	v_pk_mul_f32 v[42:43], v[64:65], s[10:11] op_sel_hi:[1,0]
	v_pk_mul_f32 v[46:47], v[68:69], s[10:11] op_sel_hi:[1,0]
	v_mov_b32_e32 v64, v201
	v_mov_b32_e32 v65, v201
	v_cvt_pk_fp8_f32 v137, v118, v119 op_sel:[0,0,1]
	v_pk_mul_f32 v[118:119], v[124:125], s[10:11] op_sel_hi:[1,0]
	v_mov_b32_e32 v121, v201
	v_cvt_pk_fp8_f32 v113, v102, v103 op_sel:[0,0,1]
	v_pk_mul_f32 v[102:103], v[108:109], s[10:11] op_sel_hi:[1,0]
	v_mov_b32_e32 v105, v201
	v_cvt_pk_fp8_f32 v97, v78, v79 op_sel:[0,0,1]
	v_pk_mul_f32 v[78:79], v[92:93], s[10:11] op_sel_hi:[1,0]
	v_mov_b32_e32 v89, v201
	v_cvt_pk_fp8_f32 v64, v42, v43
	v_cvt_pk_fp8_f32 v65, v46, v47
	v_pk_mul_f32 v[42:43], v[56:57], s[10:11] op_sel_hi:[1,0]
	v_pk_mul_f32 v[46:47], v[60:61], s[10:11] op_sel_hi:[1,0]
	v_mov_b32_e32 v56, v201
	v_mov_b32_e32 v57, v201
	v_cvt_pk_fp8_f32 v121, v118, v119
	v_cvt_pk_fp8_f32 v105, v102, v103
	v_cvt_pk_fp8_f32 v89, v78, v79
	v_cvt_pk_fp8_f32 v56, v42, v43
	v_cvt_pk_fp8_f32 v57, v46, v47
	v_pk_mul_f32 v[40:41], v[66:67], s[10:11] op_sel_hi:[1,0]
	v_pk_mul_f32 v[44:45], v[70:71], s[10:11] op_sel_hi:[1,0]
	v_pk_mul_f32 v[116:117], v[126:127], s[10:11] op_sel_hi:[1,0]
	v_pk_mul_f32 v[100:101], v[110:111], s[10:11] op_sel_hi:[1,0]
	v_pk_mul_f32 v[76:77], v[94:95], s[10:11] op_sel_hi:[1,0]
	v_cvt_pk_fp8_f32 v64, v40, v41 op_sel:[0,0,1]
	v_cvt_pk_fp8_f32 v65, v44, v45 op_sel:[0,0,1]
	v_pk_mul_f32 v[40:41], v[58:59], s[10:11] op_sel_hi:[1,0]
	v_pk_mul_f32 v[44:45], v[62:63], s[10:11] op_sel_hi:[1,0]
	v_cvt_pk_fp8_f32 v121, v116, v117 op_sel:[0,0,1]
	v_cvt_pk_fp8_f32 v105, v100, v101 op_sel:[0,0,1]
	v_cvt_pk_fp8_f32 v89, v76, v77 op_sel:[0,0,1]
	v_cvt_pk_fp8_f32 v56, v40, v41 op_sel:[0,0,1]
	v_cvt_pk_fp8_f32 v57, v44, v45 op_sel:[0,0,1]
	s_add_u32 s8, s68, s46
	s_addc_u32 s9, s69, 0
	v_or_b32_e32 v74, 0xc000, v135
	v_or_b32_e32 v114, 0x4000, v135
	v_or_b32_e32 v98, 0x8000, v135
	global_store_dwordx2 v74, v[64:65], s[8:9] offset:128
	v_add_u32_e32 v64, 0x20000, v135
	global_store_dwordx2 v135, v[136:137], s[8:9]
	global_store_dwordx2 v135, v[120:121], s[8:9] offset:128
	global_store_dwordx2 v114, v[112:113], s[8:9]
	global_store_dwordx2 v114, v[104:105], s[8:9] offset:128
	global_store_dwordx2 v98, v[96:97], s[8:9]
	global_store_dwordx2 v98, v[88:89], s[8:9] offset:128
	global_store_dwordx2 v74, v[72:73], s[8:9]
	global_store_dwordx2 v64, v[56:57], s[8:9]
	v_pk_mul_f32 v[42:43], v[80:81], s[10:11] op_sel_hi:[1,0]
	v_mov_b32_e32 v56, v201
	v_cvt_pk_fp8_f32 v56, v42, v43
	v_pk_mul_f32 v[40:41], v[82:83], s[10:11] op_sel_hi:[1,0]
	v_pk_mul_f32 v[46:47], v[84:85], s[10:11] op_sel_hi:[1,0]
	v_mov_b32_e32 v57, v201
	v_cvt_pk_fp8_f32 v56, v40, v41 op_sel:[0,0,1]
	v_pk_mul_f32 v[32:33], v[32:33], s[10:11] op_sel_hi:[1,0]
	v_pk_mul_f32 v[36:37], v[36:37], s[10:11] op_sel_hi:[1,0]
	v_mov_b32_e32 v40, v201
	v_mov_b32_e32 v41, v201
	v_cvt_pk_fp8_f32 v57, v46, v47
	v_cvt_pk_fp8_f32 v40, v32, v33
	v_cvt_pk_fp8_f32 v41, v36, v37
	v_pk_mul_f32 v[44:45], v[86:87], s[10:11] op_sel_hi:[1,0]
	v_pk_mul_f32 v[34:35], v[34:35], s[10:11] op_sel_hi:[1,0]
	v_pk_mul_f32 v[38:39], v[38:39], s[10:11] op_sel_hi:[1,0]
	v_cvt_pk_fp8_f32 v57, v44, v45 op_sel:[0,0,1]
	v_cvt_pk_fp8_f32 v40, v34, v35 op_sel:[0,0,1]
	v_cvt_pk_fp8_f32 v41, v38, v39 op_sel:[0,0,1]
	v_add_u32_e32 v42, 0x24000, v135
	global_store_dwordx2 v64, v[56:57], s[8:9] offset:128
	v_pk_mul_f32 v[34:35], v[48:49], s[10:11] op_sel_hi:[1,0]
	global_store_dwordx2 v42, v[40:41], s[8:9]
	v_mov_b32_e32 v40, v201
	v_cvt_pk_fp8_f32 v40, v34, v35
	v_pk_mul_f32 v[32:33], v[50:51], s[10:11] op_sel_hi:[1,0]
	v_pk_mul_f32 v[16:17], v[16:17], s[10:11] op_sel_hi:[1,0]
	v_pk_mul_f32 v[18:19], v[18:19], s[10:11] op_sel_hi:[1,0]
	v_cvt_pk_fp8_f32 v40, v32, v33 op_sel:[0,0,1]
	v_mov_b32_e32 v32, v201
	v_cvt_pk_fp8_f32 v32, v16, v17
	v_pk_mul_f32 v[16:17], v[26:27], s[10:11] op_sel_hi:[1,0]
	v_pk_mul_f32 v[20:21], v[20:21], s[10:11] op_sel_hi:[1,0]
	v_mov_b32_e32 v33, v201
	v_cvt_pk_fp8_f32 v32, v18, v19 op_sel:[0,0,1]
	v_pk_mul_f32 v[18:19], v[24:25], s[10:11] op_sel_hi:[1,0]
	v_mov_b32_e32 v24, v201
	v_cvt_pk_fp8_f32 v24, v18, v19
	v_pk_mul_f32 v[0:1], v[0:1], s[10:11] op_sel_hi:[1,0]
	v_pk_mul_f32 v[4:5], v[4:5], s[10:11] op_sel_hi:[1,0]
	v_cvt_pk_fp8_f32 v33, v20, v21
	v_cvt_pk_fp8_f32 v24, v16, v17 op_sel:[0,0,1]
	v_mov_b32_e32 v16, v201
	v_mov_b32_e32 v17, v201
	v_cvt_pk_fp8_f32 v16, v0, v1
	v_cvt_pk_fp8_f32 v17, v4, v5
	v_pk_mul_f32 v[22:23], v[22:23], s[10:11] op_sel_hi:[1,0]
	v_pk_mul_f32 v[2:3], v[2:3], s[10:11] op_sel_hi:[1,0]
	v_pk_mul_f32 v[6:7], v[6:7], s[10:11] op_sel_hi:[1,0]
	v_pk_mul_f32 v[38:39], v[52:53], s[10:11] op_sel_hi:[1,0]
	v_mov_b32_e32 v41, v201
	v_cvt_pk_fp8_f32 v33, v22, v23 op_sel:[0,0,1]
	v_pk_mul_f32 v[22:23], v[28:29], s[10:11] op_sel_hi:[1,0]
	v_mov_b32_e32 v25, v201
	v_cvt_pk_fp8_f32 v16, v2, v3 op_sel:[0,0,1]
	v_cvt_pk_fp8_f32 v17, v6, v7 op_sel:[0,0,1]
	v_pk_mul_f32 v[2:3], v[8:9], s[10:11] op_sel_hi:[1,0]
	v_pk_mul_f32 v[6:7], v[12:13], s[10:11] op_sel_hi:[1,0]
	v_mov_b32_e32 v8, v201
	v_mov_b32_e32 v9, v201
	v_cvt_pk_fp8_f32 v41, v38, v39
	v_cvt_pk_fp8_f32 v25, v22, v23
	v_cvt_pk_fp8_f32 v8, v2, v3
	v_cvt_pk_fp8_f32 v9, v6, v7
	v_pk_mul_f32 v[36:37], v[54:55], s[10:11] op_sel_hi:[1,0]
	v_pk_mul_f32 v[20:21], v[30:31], s[10:11] op_sel_hi:[1,0]
	v_pk_mul_f32 v[0:1], v[10:11], s[10:11] op_sel_hi:[1,0]
	v_pk_mul_f32 v[4:5], v[14:15], s[10:11] op_sel_hi:[1,0]
	v_cvt_pk_fp8_f32 v41, v36, v37 op_sel:[0,0,1]
	v_cvt_pk_fp8_f32 v25, v20, v21 op_sel:[0,0,1]
	v_cvt_pk_fp8_f32 v8, v0, v1 op_sel:[0,0,1]
	v_cvt_pk_fp8_f32 v9, v4, v5 op_sel:[0,0,1]
	v_add_u32_e32 v34, 0x28000, v135
	v_add_u32_e32 v18, 0x2c000, v135
	global_store_dwordx2 v42, v[40:41], s[8:9] offset:128
	global_store_dwordx2 v34, v[32:33], s[8:9]
	global_store_dwordx2 v34, v[24:25], s[8:9] offset:128
	global_store_dwordx2 v18, v[16:17], s[8:9]
	global_store_dwordx2 v18, v[8:9], s[8:9] offset:128
	s_mov_b64 s[8:9], -1
	s_andn2_b64 vcc, exec, s[6:7]
	s_cbranch_vccnz .LBB0_582
	s_andn2_b64 vcc, exec, s[2:3]
	v_mov_b64 v[112:113], 0
	v_mov_b64 v[114:115], 0
	v_mov_b64 v[116:117], 0
	v_mov_b64 v[118:119], 0
	v_mov_b64 v[96:97], 0
	v_mov_b64 v[98:99], 0
	v_mov_b64 v[100:101], 0
	v_mov_b64 v[102:103], 0
	v_mov_b64 v[72:73], 0
	v_mov_b64 v[74:75], 0
	v_mov_b64 v[76:77], 0
	v_mov_b64 v[78:79], 0
	v_mov_b64 v[40:41], 0
	v_mov_b64 v[42:43], 0
	v_mov_b64 v[44:45], 0
	v_mov_b64 v[46:47], 0
	v_mov_b64 v[120:121], 0
	v_mov_b64 v[122:123], 0
	v_mov_b64 v[124:125], 0
	v_mov_b64 v[126:127], 0
	v_mov_b64 v[104:105], 0
	v_mov_b64 v[106:107], 0
	v_mov_b64 v[108:109], 0
	v_mov_b64 v[110:111], 0
	v_mov_b64 v[88:89], 0
	v_mov_b64 v[90:91], 0
	v_mov_b64 v[92:93], 0
	v_mov_b64 v[94:95], 0
	v_mov_b64 v[64:65], 0
	v_mov_b64 v[66:67], 0
	v_mov_b64 v[68:69], 0
	v_mov_b64 v[70:71], 0
	v_mov_b64 v[56:57], 0
	v_mov_b64 v[58:59], 0
	v_mov_b64 v[60:61], 0
	v_mov_b64 v[62:63], 0
	v_mov_b64 v[32:33], 0
	v_mov_b64 v[34:35], 0
	v_mov_b64 v[36:37], 0
	v_mov_b64 v[38:39], 0
	v_mov_b64 v[16:17], 0
	v_mov_b64 v[18:19], 0
	v_mov_b64 v[20:21], 0
	v_mov_b64 v[22:23], 0
	v_mov_b64 v[0:1], 0
	v_mov_b64 v[2:3], 0
	v_mov_b64 v[4:5], 0
	v_mov_b64 v[6:7], 0
	v_mov_b64 v[80:81], 0
	v_mov_b64 v[82:83], 0
	v_mov_b64 v[84:85], 0
	v_mov_b64 v[86:87], 0
	v_mov_b64 v[48:49], 0
	v_mov_b64 v[50:51], 0
	v_mov_b64 v[52:53], 0
	v_mov_b64 v[54:55], 0
	v_mov_b64 v[24:25], 0
	v_mov_b64 v[26:27], 0
	v_mov_b64 v[28:29], 0
	v_mov_b64 v[30:31], 0
	v_mov_b64 v[8:9], 0
	v_mov_b64 v[10:11], 0
	v_mov_b64 v[12:13], 0
	v_mov_b64 v[14:15], 0
	s_cbranch_vccnz .LBB0_581
	s_barrier
	s_branch .LBB0_581

.LBB0_669:
	s_lshl_b32 s10, s75, 5
	s_and_b32 s38, s10, 0x60
	v_and_b32_e32 v1, 15, v0
	v_and_b32_e32 v2, 48, v0
	v_lshlrev_b32_e32 v0, 2, v0
	s_lshl_b32 s10, s38, 7
	v_lshl_or_b32 v1, v1, 6, v2
	v_and_b32_e32 v0, 32, v0
	s_lshl_b32 s6, s6, 8
	s_lshl_b32 s3, s3, 13
	v_bitop3_b32 v157, v1, s10, v0 bitop3:0xde
	v_readlane_b32 s10, v254, 30
	s_add_i32 s14, s16, s6
	v_bitop3_b32 v128, v1, s3, v0 bitop3:0xde
	v_readlane_b32 s11, v254, 31
	s_add_i32 s3, s70, 1
	s_and_b64 s[4:5], exec, s[4:5]
	v_cndmask_b32_e64 v0, 0, 1, s[10:11]
	s_waitcnt vmcnt(2)
	s_barrier
	v_readfirstlane_b32 s4, v0
	s_cselect_b32 s3, s4, s3
	s_lshl_b32 s36, s3, 10
	s_lshl_b64 s[4:5], s[36:37], 2
	s_add_u32 s3, s76, s4
	s_addc_u32 s4, s77, s5
	s_add_u32 s39, s3, 0x9f720000
	s_addc_u32 s40, s4, 0
	s_add_u32 s41, s76, 0x5c400000
	s_addc_u32 s42, s77, 0
	s_add_i32 s43, s25, 0x18000
	s_add_i32 s44, s25, 0x1a000
	s_add_i32 s45, s25, 0x8000
	s_add_i32 s46, s25, 0xa000
	s_add_i32 s47, s25, 0x1c000
	s_add_i32 s48, s25, 0x1e000
	s_add_i32 s49, s91, 0x10000
	s_add_i32 s50, s91, 0x14000
	s_add_i32 s51, s25, 0xc000
	s_add_i32 s52, s91, 0x18000
	s_add_i32 s53, s91, 0x1c000
	s_cmp_lt_u32 s75, 4
	s_cselect_b64 s[10:11], -1, 0
	s_lshl_b32 s3, s75, 4
	s_and_b32 s54, s3, 0x3fffc0
	v_readlane_b32 s3, v254, 34
	s_add_i32 s55, s25, 0xe000
	s_ashr_i32 s56, s3, 31
	s_add_u32 s4, s12, 0x80
	s_addc_u32 s5, s13, 0
	s_mov_b32 m0, s43
	s_nop 4
	global_load_lds_dwordx4 v154, s[4:5]
	s_mov_b32 m0, s44
	s_nop 4
	global_load_lds_dwordx4 v156, s[4:5]
	s_add_u32 s4, s18, 0x80
	s_addc_u32 s5, s19, 0
	s_mov_b32 m0, s45
	s_nop 4
	global_load_lds_dwordx4 v153, s[4:5]
	s_mov_b32 m0, s46
	s_nop 4
	global_load_lds_dwordx4 v155, s[4:5]
	s_or_b32 s4, s7, 0x20080
	s_add_u32 s4, s20, s4
	s_addc_u32 s5, s21, 0
	s_mov_b32 m0, s47
	s_nop 4
	global_load_lds_dwordx4 v154, s[4:5]
	s_mov_b32 m0, s48
	s_nop 4
	global_load_lds_dwordx4 v156, s[4:5]
	s_waitcnt vmcnt(6)
	s_waitcnt lgkmcnt(0)
	s_cmp_lg_u64 s[0:1], 0
	s_cselect_b64 s[12:13], -1, 0
	s_add_u32 s57, s22, 0x20080
	s_mov_b32 s3, s37
	s_addc_u32 s58, s23, 0
	s_mov_b32 s59, 0
	v_add_u32_e32 v158, s91, v128
	s_mov_b32 s36, s14
	s_mov_b32 s61, s7
	s_barrier
	v_mov_b64 v[120:121], 0
	v_mov_b64 v[122:123], 0
	v_mov_b64 v[124:125], 0
	v_mov_b64 v[126:127], 0
	v_mov_b64 v[108:109], 0
	v_mov_b64 v[110:111], 0
	v_mov_b64 v[116:117], 0
	v_mov_b64 v[118:119], 0
	v_mov_b64 v[92:93], 0
	v_mov_b64 v[94:95], 0
	v_mov_b64 v[100:101], 0
	v_mov_b64 v[102:103], 0
	s_waitcnt vmcnt(6)
	v_mov_b64 v[76:77], 0
	v_mov_b64 v[78:79], 0
	v_mov_b64 v[84:85], 0
	v_mov_b64 v[86:87], 0
	s_waitcnt vmcnt(17)
	v_mov_b64 v[28:29], 0
	s_waitcnt vmcnt(16)
	v_mov_b64 v[30:31], 0
	v_mov_b64 v[0:1], 0
	v_mov_b64 v[2:3], 0
	v_mov_b64 v[16:17], 0
	v_mov_b64 v[18:19], 0
	v_mov_b64 v[4:5], 0
	v_mov_b64 v[6:7], 0
	v_mov_b64 v[20:21], 0
	v_mov_b64 v[22:23], 0
	v_mov_b64 v[8:9], 0
	v_mov_b64 v[10:11], 0
	v_mov_b64 v[24:25], 0
	v_mov_b64 v[26:27], 0
	v_mov_b64 v[12:13], 0
	v_mov_b64 v[14:15], 0
	v_mov_b64 v[104:105], 0
	v_mov_b64 v[106:107], 0
	v_mov_b64 v[112:113], 0
	v_mov_b64 v[114:115], 0
	v_mov_b64 v[88:89], 0
	v_mov_b64 v[90:91], 0
	v_mov_b64 v[96:97], 0
	v_mov_b64 v[98:99], 0
	s_waitcnt vmcnt(4)
	v_mov_b64 v[72:73], 0
	v_mov_b64 v[74:75], 0
	v_mov_b64 v[80:81], 0
	v_mov_b64 v[82:83], 0
	v_mov_b64 v[64:65], 0
	v_mov_b64 v[66:67], 0
	v_mov_b64 v[68:69], 0
	v_mov_b64 v[70:71], 0
	s_waitcnt vmcnt(1)
	v_mov_b64 v[48:49], 0
	s_waitcnt vmcnt(6)
	v_mov_b64 v[50:51], 0
	v_mov_b64 v[32:33], 0
	v_mov_b64 v[34:35], 0
	s_waitcnt vmcnt(5)
	v_mov_b64 v[52:53], 0
	s_waitcnt vmcnt(4)
	v_mov_b64 v[54:55], 0
	v_mov_b64 v[36:37], 0
	v_mov_b64 v[38:39], 0
	s_waitcnt vmcnt(0)
	v_mov_b64 v[56:57], 0
	s_waitcnt vmcnt(2)
	v_mov_b64 v[58:59], 0
	v_mov_b64 v[40:41], 0
	v_mov_b64 v[42:43], 0
	s_waitcnt vmcnt(1)
	v_mov_b64 v[60:61], 0
	s_waitcnt vmcnt(0)
	v_mov_b64 v[62:63], 0
	v_mov_b64 v[44:45], 0
	v_mov_b64 v[46:47], 0
	s_branch .LBB0_672

.LBB0_686:
	global_load_dwordx4 v[86:89], v[148:149], off offset:528
	s_add_u32 s6, s14, 0x100
	s_waitcnt vmcnt(1)
	v_pk_fma_f32 v[28:29], v[28:29], v[72:73], v[68:69]
	s_addc_u32 s7, s15, 0
	v_pk_fma_f32 v[30:31], v[30:31], v[74:75], v[70:71]
	v_pk_fma_f32 v[82:83], v[18:19], v[74:75], v[70:71]
	v_pk_fma_f32 v[90:91], v[16:17], v[72:73], v[68:69]
	v_cvt_pk_bf16_f32 v16, v28, v29
	v_cvt_pk_bf16_f32 v17, v30, v31
	v_lshl_add_u64 v[28:29], v[200:201], 1, s[6:7]
	v_pk_fma_f32 v[22:23], v[22:23], v[74:75], v[70:71]
	v_pk_fma_f32 v[20:21], v[20:21], v[72:73], v[68:69]
	v_lshl_add_u64 v[30:31], v[108:109], 1, s[6:7]
	v_pk_fma_f32 v[26:27], v[26:27], v[74:75], v[70:71]
	v_pk_fma_f32 v[24:25], v[24:25], v[72:73], v[68:69]
	v_pk_fma_f32 v[48:49], v[48:49], v[72:73], v[68:69]
	v_pk_fma_f32 v[52:53], v[52:53], v[72:73], v[68:69]
	v_pk_fma_f32 v[56:57], v[56:57], v[72:73], v[68:69]
	v_pk_fma_f32 v[60:61], v[60:61], v[72:73], v[68:69]
	v_lshl_add_u64 v[68:69], v[92:93], 1, s[6:7]
	v_pk_fma_f32 v[50:51], v[50:51], v[74:75], v[70:71]
	v_pk_fma_f32 v[54:55], v[54:55], v[74:75], v[70:71]
	v_pk_fma_f32 v[58:59], v[58:59], v[74:75], v[70:71]
	v_pk_fma_f32 v[62:63], v[62:63], v[74:75], v[70:71]
	s_andn2_b64 vcc, exec, s[4:5]
	s_mov_b64 s[4:5], -1
	s_waitcnt vmcnt(0)
	v_pk_fma_f32 v[2:3], v[2:3], v[88:89], v[66:67]
	v_pk_fma_f32 v[0:1], v[0:1], v[86:87], v[64:65]
	v_pk_fma_f32 v[6:7], v[6:7], v[88:89], v[66:67]
	v_pk_fma_f32 v[4:5], v[4:5], v[86:87], v[64:65]
	v_cvt_pk_bf16_f32 v18, v0, v1
	v_cvt_pk_bf16_f32 v19, v2, v3
	global_store_dwordx4 v[144:145], v[16:19], off offset:256
	v_cvt_pk_bf16_f32 v0, v90, v91
	v_cvt_pk_bf16_f32 v1, v82, v83
	v_cvt_pk_bf16_f32 v2, v4, v5
	v_cvt_pk_bf16_f32 v3, v6, v7
	v_pk_fma_f32 v[10:11], v[10:11], v[88:89], v[66:67]
	v_pk_fma_f32 v[8:9], v[8:9], v[86:87], v[64:65]
	global_store_dwordx4 v[28:29], v[0:3], off
	v_pk_fma_f32 v[14:15], v[14:15], v[88:89], v[66:67]
	v_pk_fma_f32 v[12:13], v[12:13], v[86:87], v[64:65]
	v_cvt_pk_bf16_f32 v0, v20, v21
	v_cvt_pk_bf16_f32 v1, v22, v23
	v_cvt_pk_bf16_f32 v2, v8, v9
	v_cvt_pk_bf16_f32 v3, v10, v11
	global_store_dwordx4 v[30:31], v[0:3], off
	v_pk_fma_f32 v[34:35], v[34:35], v[88:89], v[66:67]
	v_pk_fma_f32 v[32:33], v[32:33], v[86:87], v[64:65]
	v_cvt_pk_bf16_f32 v0, v24, v25
	v_cvt_pk_bf16_f32 v1, v26, v27
	v_cvt_pk_bf16_f32 v2, v12, v13
	v_cvt_pk_bf16_f32 v3, v14, v15
	global_store_dwordx4 v[68:69], v[0:3], off
	v_pk_fma_f32 v[38:39], v[38:39], v[88:89], v[66:67]
	v_pk_fma_f32 v[36:37], v[36:37], v[86:87], v[64:65]
	v_cvt_pk_bf16_f32 v0, v48, v49
	v_cvt_pk_bf16_f32 v1, v50, v51
	v_cvt_pk_bf16_f32 v2, v32, v33
	v_cvt_pk_bf16_f32 v3, v34, v35
	global_store_dwordx4 v[76:77], v[0:3], off offset:256
	v_pk_fma_f32 v[42:43], v[42:43], v[88:89], v[66:67]
	v_pk_fma_f32 v[40:41], v[40:41], v[86:87], v[64:65]
	v_cvt_pk_bf16_f32 v0, v52, v53
	v_cvt_pk_bf16_f32 v1, v54, v55
	v_cvt_pk_bf16_f32 v2, v36, v37
	v_cvt_pk_bf16_f32 v3, v38, v39
	global_store_dwordx4 v[78:79], v[0:3], off offset:256
	v_pk_fma_f32 v[46:47], v[46:47], v[88:89], v[66:67]
	v_pk_fma_f32 v[44:45], v[44:45], v[86:87], v[64:65]
	v_cvt_pk_bf16_f32 v0, v56, v57
	v_cvt_pk_bf16_f32 v1, v58, v59
	v_cvt_pk_bf16_f32 v2, v40, v41
	v_cvt_pk_bf16_f32 v3, v42, v43
	global_store_dwordx4 v[84:85], v[0:3], off offset:256
	s_nop 1
	v_cvt_pk_bf16_f32 v0, v60, v61
	v_cvt_pk_bf16_f32 v1, v62, v63
	v_cvt_pk_bf16_f32 v2, v44, v45
	v_cvt_pk_bf16_f32 v3, v46, v47
	global_store_dwordx4 v[80:81], v[0:3], off offset:256
	s_cbranch_vccnz .LBB0_671
	s_andn2_b64 vcc, exec, s[8:9]
	v_mov_b64 v[120:121], 0
	v_mov_b64 v[122:123], 0
	v_mov_b64 v[124:125], 0
	v_mov_b64 v[126:127], 0
	v_mov_b64 v[108:109], 0
	v_mov_b64 v[110:111], 0
	v_mov_b64 v[116:117], 0
	v_mov_b64 v[118:119], 0
	v_mov_b64 v[92:93], 0
	v_mov_b64 v[94:95], 0
	v_mov_b64 v[100:101], 0
	v_mov_b64 v[102:103], 0
	v_mov_b64 v[76:77], 0
	v_mov_b64 v[78:79], 0
	v_mov_b64 v[84:85], 0
	v_mov_b64 v[86:87], 0
	v_mov_b64 v[28:29], 0
	v_mov_b64 v[30:31], 0
	v_mov_b64 v[0:1], 0
	v_mov_b64 v[2:3], 0
	v_mov_b64 v[16:17], 0
	v_mov_b64 v[18:19], 0
	v_mov_b64 v[4:5], 0
	v_mov_b64 v[6:7], 0
	v_mov_b64 v[20:21], 0
	v_mov_b64 v[22:23], 0
	v_mov_b64 v[8:9], 0
	v_mov_b64 v[10:11], 0
	v_mov_b64 v[24:25], 0
	v_mov_b64 v[26:27], 0
	v_mov_b64 v[12:13], 0
	v_mov_b64 v[14:15], 0
	v_mov_b64 v[104:105], 0
	v_mov_b64 v[106:107], 0
	v_mov_b64 v[112:113], 0
	v_mov_b64 v[114:115], 0
	v_mov_b64 v[88:89], 0
	v_mov_b64 v[90:91], 0
	v_mov_b64 v[96:97], 0
	v_mov_b64 v[98:99], 0
	v_mov_b64 v[72:73], 0
	v_mov_b64 v[74:75], 0
	v_mov_b64 v[80:81], 0
	v_mov_b64 v[82:83], 0
	v_mov_b64 v[64:65], 0
	v_mov_b64 v[66:67], 0
	v_mov_b64 v[68:69], 0
	v_mov_b64 v[70:71], 0
	v_mov_b64 v[48:49], 0
	v_mov_b64 v[50:51], 0
	v_mov_b64 v[32:33], 0
	v_mov_b64 v[34:35], 0
	v_mov_b64 v[52:53], 0
	v_mov_b64 v[54:55], 0
	v_mov_b64 v[36:37], 0
	v_mov_b64 v[38:39], 0
	v_mov_b64 v[56:57], 0
	v_mov_b64 v[58:59], 0
	v_mov_b64 v[40:41], 0
	v_mov_b64 v[42:43], 0
	v_mov_b64 v[60:61], 0
	v_mov_b64 v[62:63], 0
	v_mov_b64 v[44:45], 0
	v_mov_b64 v[46:47], 0
	s_cbranch_vccnz .LBB0_670
	s_barrier
	s_branch .LBB0_670

.LBB0_1009:
	s_lshl_b32 s10, s10, 8
	s_add_i32 s62, s10, s63
	s_add_u32 s31, s76, 0x8b000000
	s_addc_u32 s33, s77, 0
	s_lshl_b64 s[14:15], s[36:37], 2
	s_add_u32 s34, s6, s14
	s_addc_u32 s35, s7, s15
	s_add_u32 s6, s76, s14
	s_addc_u32 s7, s77, s15
	s_add_u32 s36, s6, 0x9f600000
	s_addc_u32 s38, s7, 0
	s_lshl_b32 s6, s75, 5
	s_and_b32 s39, s6, 0x60
	s_lshl_b32 s9, s9, 13
	s_lshl_b32 s11, s39, 7
	s_add_i32 s40, s23, 0x18000
	s_add_i32 s41, s23, 0x1a000
	s_add_i32 s42, s23, 0x8000
	s_add_i32 s43, s23, 0xa000
	s_add_i32 s44, s23, 0x1c000
	s_add_i32 s45, s23, 0x1e000
	s_add_i32 s46, s91, 0x10000
	s_add_i32 s47, s91, 0x14000
	s_add_i32 s48, s23, 0xc000
	s_add_i32 s49, s91, 0x18000
	s_add_i32 s50, s91, 0x1c000
	s_cmp_lt_u32 s75, 4
	s_cselect_b64 s[6:7], -1, 0
	s_lshl_b32 s14, s75, 4
	s_and_b32 s51, s14, 0x3fffc0
	v_readlane_b32 s14, v254, 34
	v_readlane_b32 s15, v254, 35
	s_add_i32 s52, s23, 0xe000
	s_ashr_i32 s53, s14, 31
	s_ashr_i32 s54, s15, 31
	s_ashr_i32 s55, s14, 3
	s_add_u32 s4, s4, 0x80
	s_waitcnt vmcnt(2)
	s_barrier
	s_addc_u32 s5, s5, 0
	s_mov_b32 m0, s40
	s_nop 4
	global_load_lds_dwordx4 v146, s[4:5]
	s_mov_b32 m0, s41
	s_nop 4
	global_load_lds_dwordx4 v148, s[4:5]
	s_add_u32 s4, s12, 0x80
	s_addc_u32 s5, s13, 0
	s_mov_b32 m0, s42
	s_nop 4
	global_load_lds_dwordx4 v145, s[4:5]
	s_mov_b32 m0, s43
	s_nop 4
	global_load_lds_dwordx4 v147, s[4:5]
	s_or_b32 s4, s64, 0x20080
	s_add_u32 s4, s21, s4
	s_addc_u32 s5, s22, 0
	s_mov_b32 m0, s44
	s_nop 4
	global_load_lds_dwordx4 v146, s[4:5]
	v_and_b32_e32 v1, 15, v0
	v_and_b32_e32 v2, 48, v0
	v_lshlrev_b32_e32 v0, 2, v0
	s_mov_b32 m0, s45
	s_nop 4
	global_load_lds_dwordx4 v148, s[4:5]
	v_lshl_or_b32 v1, v1, 6, v2
	v_and_b32_e32 v0, 32, v0
	s_waitcnt vmcnt(6)
	v_bitop3_b32 v128, v1, s9, v0 bitop3:0xde
	v_bitop3_b32 v149, v1, s11, v0 bitop3:0xde
	s_mov_b32 s9, 0
	v_add_u32_e32 v150, s91, v128
	s_barrier
	v_mov_b64 v[104:105], 0
	v_mov_b64 v[106:107], 0
	v_mov_b64 v[112:113], 0
	v_mov_b64 v[114:115], 0
	v_mov_b64 v[120:121], 0
	v_mov_b64 v[122:123], 0
	v_mov_b64 v[124:125], 0
	v_mov_b64 v[126:127], 0
	s_waitcnt vmcnt(7)
	v_mov_b64 v[68:69], 0
	v_mov_b64 v[70:71], 0
	s_waitcnt vmcnt(6)
	v_mov_b64 v[76:77], 0
	v_mov_b64 v[78:79], 0
	v_mov_b64 v[84:85], 0
	v_mov_b64 v[86:87], 0
	v_mov_b64 v[92:93], 0
	v_mov_b64 v[94:95], 0
	v_mov_b64 v[40:41], 0
	v_mov_b64 v[42:43], 0
	s_waitcnt vmcnt(1)
	v_mov_b64 v[48:49], 0
	v_mov_b64 v[50:51], 0
	s_waitcnt vmcnt(0)
	v_mov_b64 v[56:57], 0
	v_mov_b64 v[58:59], 0
	v_mov_b64 v[60:61], 0
	v_mov_b64 v[62:63], 0
	v_mov_b64 v[8:9], 0
	v_mov_b64 v[10:11], 0
	v_mov_b64 v[16:17], 0
	v_mov_b64 v[18:19], 0
	v_mov_b64 v[24:25], 0
	v_mov_b64 v[26:27], 0
	v_mov_b64 v[28:29], 0
	v_mov_b64 v[30:31], 0
	v_mov_b64 v[96:97], 0
	v_mov_b64 v[98:99], 0
	v_mov_b64 v[100:101], 0
	v_mov_b64 v[102:103], 0
	v_mov_b64 v[108:109], 0
	v_mov_b64 v[110:111], 0
	v_mov_b64 v[116:117], 0
	v_mov_b64 v[118:119], 0
	v_mov_b64 v[64:65], 0
	v_mov_b64 v[66:67], 0
	v_mov_b64 v[72:73], 0
	v_mov_b64 v[74:75], 0
	v_mov_b64 v[80:81], 0
	v_mov_b64 v[82:83], 0
	v_mov_b64 v[88:89], 0
	v_mov_b64 v[90:91], 0
	v_mov_b64 v[32:33], 0
	v_mov_b64 v[34:35], 0
	v_mov_b64 v[36:37], 0
	v_mov_b64 v[38:39], 0
	v_mov_b64 v[44:45], 0
	v_mov_b64 v[46:47], 0
	v_mov_b64 v[52:53], 0
	v_mov_b64 v[54:55], 0
	v_mov_b64 v[0:1], 0
	v_mov_b64 v[2:3], 0
	v_mov_b64 v[4:5], 0
	v_mov_b64 v[6:7], 0
	v_mov_b64 v[12:13], 0
	v_mov_b64 v[14:15], 0
	v_mov_b64 v[20:21], 0
	v_mov_b64 v[22:23], 0
	s_branch .LBB0_1012

.LBB0_1032:
	v_mbcnt_lo_u32_b32 v128, -1, 0
	v_mbcnt_hi_u32_b32 v128, -1, v128
	s_mov_b32 s10, 0x41800000
	v_lshrrev_b32_e32 v130, 1, v128
	v_and_or_b32 v130, v130, 24, s39
	v_and_b32_e32 v129, 15, v128
	v_lshl_add_u32 v131, v130, 2, s14
	v_and_b32_e32 v128, 16, v128
	v_add_u32_e32 v152, 0x20000, v131
	v_add_u32_e32 v151, 0x20400, v131
	v_cmp_eq_u32_e32 vcc, 0, v128
	v_or3_b32 v153, s51, v129, v128
	v_lshrrev_b32_e32 v128, 1, v128
	v_sub_u32_e32 v158, v130, v128
	ds_read_b128 v[132:135], v152
	ds_read_b128 v[136:139], v152 offset:16
	ds_read_b128 v[140:143], v151
	ds_read_b128 v[128:131], v151 offset:16
	s_mov_b32 s12, 0x40088889
	s_add_u32 s8, s31, s62
	s_addc_u32 s9, s33, 0
	v_lshl_add_u32 v153, v153, 10, v158
	s_waitcnt lgkmcnt(0)
	v_pk_mul_f32 v[140:141], v[140:141], s[12:13] op_sel_hi:[1,0]
	v_pk_mul_f32 v[132:133], v[132:133], s[10:11] op_sel_hi:[1,0]
	v_pk_mul_f32 v[142:143], v[142:143], s[12:13] op_sel_hi:[1,0]
	v_pk_mul_f32 v[134:135], v[134:135], s[10:11] op_sel_hi:[1,0]
	v_pk_mul_f32 v[128:129], v[128:129], s[12:13] op_sel_hi:[1,0]
	v_pk_mul_f32 v[136:137], v[136:137], s[10:11] op_sel_hi:[1,0]
	v_pk_mul_f32 v[130:131], v[130:131], s[12:13] op_sel_hi:[1,0]
	v_pk_mul_f32 v[138:139], v[138:139], s[10:11] op_sel_hi:[1,0]
	v_pk_fma_f32 v[68:69], v[68:69], v[140:141], v[132:133]
	v_pk_fma_f32 v[70:71], v[70:71], v[142:143], v[134:135]
	v_pk_fma_f32 v[76:77], v[76:77], v[128:129], v[136:137]
	v_pk_fma_f32 v[78:79], v[78:79], v[130:131], v[138:139]
	v_pk_fma_f32 v[84:85], v[84:85], v[140:141], v[132:133]
	v_pk_fma_f32 v[86:87], v[86:87], v[142:143], v[134:135]
	v_pk_fma_f32 v[92:93], v[92:93], v[128:129], v[136:137]
	v_pk_fma_f32 v[94:95], v[94:95], v[130:131], v[138:139]
	v_cvt_pk_fp8_f32 v154, v68, v69
	v_cvt_pk_fp8_f32 v155, v76, v77
	v_cvt_pk_fp8_f32 v156, v84, v85
	v_cvt_pk_fp8_f32 v157, v92, v93
	v_cvt_pk_fp8_f32 v154, v70, v71 op_sel:[0,0,1]
	v_cvt_pk_fp8_f32 v155, v78, v79 op_sel:[0,0,1]
	v_cvt_pk_fp8_f32 v156, v86, v87 op_sel:[0,0,1]
	v_cvt_pk_fp8_f32 v157, v94, v95 op_sel:[0,0,1]
	v_add_u32_e32 v158, 0x8000, v153
	s_nop 0
	v_permlane16_swap_b32_e32 v154, v156
	v_permlane16_swap_b32_e32 v155, v157
	global_store_dwordx4 v158, v[154:157], s[8:9]
	v_pk_fma_f32 v[104:105], v[104:105], v[140:141], v[132:133]
	v_pk_fma_f32 v[106:107], v[106:107], v[142:143], v[134:135]
	v_pk_fma_f32 v[112:113], v[112:113], v[128:129], v[136:137]
	v_pk_fma_f32 v[114:115], v[114:115], v[130:131], v[138:139]
	v_pk_fma_f32 v[120:121], v[120:121], v[140:141], v[132:133]
	v_pk_fma_f32 v[122:123], v[122:123], v[142:143], v[134:135]
	v_pk_fma_f32 v[124:125], v[124:125], v[128:129], v[136:137]
	v_pk_fma_f32 v[126:127], v[126:127], v[130:131], v[138:139]
	v_cvt_pk_fp8_f32 v68, v104, v105
	v_cvt_pk_fp8_f32 v69, v112, v113
	v_cvt_pk_fp8_f32 v70, v120, v121
	v_cvt_pk_fp8_f32 v71, v124, v125
	v_cvt_pk_fp8_f32 v68, v106, v107 op_sel:[0,0,1]
	v_cvt_pk_fp8_f32 v69, v114, v115 op_sel:[0,0,1]
	v_cvt_pk_fp8_f32 v70, v122, v123 op_sel:[0,0,1]
	v_cvt_pk_fp8_f32 v71, v126, v127 op_sel:[0,0,1]
	s_nop 0
	v_permlane16_swap_b32_e32 v68, v70
	v_permlane16_swap_b32_e32 v69, v71
	global_store_dwordx4 v153, v[68:71], s[8:9]
	v_pk_fma_f32 v[96:97], v[96:97], v[140:141], v[132:133]
	v_pk_fma_f32 v[98:99], v[98:99], v[142:143], v[134:135]
	v_pk_fma_f32 v[100:101], v[100:101], v[128:129], v[136:137]
	v_pk_fma_f32 v[102:103], v[102:103], v[130:131], v[138:139]
	v_pk_fma_f32 v[108:109], v[108:109], v[140:141], v[132:133]
	v_pk_fma_f32 v[110:111], v[110:111], v[142:143], v[134:135]
	v_pk_fma_f32 v[116:117], v[116:117], v[128:129], v[136:137]
	v_pk_fma_f32 v[118:119], v[118:119], v[130:131], v[138:139]
	v_cvt_pk_fp8_f32 v154, v96, v97
	v_cvt_pk_fp8_f32 v155, v100, v101
	v_cvt_pk_fp8_f32 v156, v108, v109
	v_cvt_pk_fp8_f32 v157, v116, v117
	v_cvt_pk_fp8_f32 v154, v98, v99 op_sel:[0,0,1]
	v_cvt_pk_fp8_f32 v155, v102, v103 op_sel:[0,0,1]
	v_cvt_pk_fp8_f32 v156, v110, v111 op_sel:[0,0,1]
	v_cvt_pk_fp8_f32 v157, v118, v119 op_sel:[0,0,1]
	v_add_u32_e32 v158, 0x20000, v153
	s_nop 0
	v_permlane16_swap_b32_e32 v154, v156
	v_permlane16_swap_b32_e32 v155, v157
	global_store_dwordx4 v158, v[154:157], s[8:9]
	v_pk_fma_f32 v[64:65], v[64:65], v[140:141], v[132:133]
	v_pk_fma_f32 v[66:67], v[66:67], v[142:143], v[134:135]
	v_pk_fma_f32 v[72:73], v[72:73], v[128:129], v[136:137]
	v_pk_fma_f32 v[74:75], v[74:75], v[130:131], v[138:139]
	v_pk_fma_f32 v[80:81], v[80:81], v[140:141], v[132:133]
	v_pk_fma_f32 v[82:83], v[82:83], v[142:143], v[134:135]
	v_pk_fma_f32 v[88:89], v[88:89], v[128:129], v[136:137]
	v_pk_fma_f32 v[90:91], v[90:91], v[130:131], v[138:139]
	v_cvt_pk_fp8_f32 v68, v64, v65
	v_cvt_pk_fp8_f32 v69, v72, v73
	v_cvt_pk_fp8_f32 v70, v80, v81
	v_cvt_pk_fp8_f32 v71, v88, v89
	v_cvt_pk_fp8_f32 v68, v66, v67 op_sel:[0,0,1]
	v_cvt_pk_fp8_f32 v69, v74, v75 op_sel:[0,0,1]
	v_cvt_pk_fp8_f32 v70, v82, v83 op_sel:[0,0,1]
	v_cvt_pk_fp8_f32 v71, v90, v91 op_sel:[0,0,1]
	v_add_u32_e32 v158, 0x28000, v153
	s_nop 0
	v_permlane16_swap_b32_e32 v68, v70
	v_permlane16_swap_b32_e32 v69, v71
	global_store_dwordx4 v158, v[68:71], s[8:9]
	ds_read_b128 v[132:135], v152 offset:512
	ds_read_b128 v[136:139], v152 offset:528
	ds_read_b128 v[140:143], v151 offset:512
	ds_read_b128 v[128:131], v151 offset:528
	s_waitcnt lgkmcnt(0)
	v_pk_mul_f32 v[140:141], v[140:141], s[12:13] op_sel_hi:[1,0]
	v_pk_mul_f32 v[132:133], v[132:133], s[10:11] op_sel_hi:[1,0]
	v_pk_mul_f32 v[142:143], v[142:143], s[12:13] op_sel_hi:[1,0]
	v_pk_mul_f32 v[134:135], v[134:135], s[10:11] op_sel_hi:[1,0]
	v_pk_mul_f32 v[128:129], v[128:129], s[12:13] op_sel_hi:[1,0]
	v_pk_mul_f32 v[136:137], v[136:137], s[10:11] op_sel_hi:[1,0]
	v_pk_mul_f32 v[130:131], v[130:131], s[12:13] op_sel_hi:[1,0]
	v_pk_mul_f32 v[138:139], v[138:139], s[10:11] op_sel_hi:[1,0]
	v_pk_fma_f32 v[40:41], v[40:41], v[140:141], v[132:133]
	v_pk_fma_f32 v[42:43], v[42:43], v[142:143], v[134:135]
	v_pk_fma_f32 v[48:49], v[48:49], v[128:129], v[136:137]
	v_pk_fma_f32 v[50:51], v[50:51], v[130:131], v[138:139]
	v_pk_fma_f32 v[56:57], v[56:57], v[140:141], v[132:133]
	v_pk_fma_f32 v[58:59], v[58:59], v[142:143], v[134:135]
	v_pk_fma_f32 v[60:61], v[60:61], v[128:129], v[136:137]
	v_pk_fma_f32 v[62:63], v[62:63], v[130:131], v[138:139]
	v_cvt_pk_fp8_f32 v154, v40, v41
	v_cvt_pk_fp8_f32 v155, v48, v49
	v_cvt_pk_fp8_f32 v156, v56, v57
	v_cvt_pk_fp8_f32 v157, v60, v61
	v_cvt_pk_fp8_f32 v154, v42, v43 op_sel:[0,0,1]
	v_cvt_pk_fp8_f32 v155, v50, v51 op_sel:[0,0,1]
	v_cvt_pk_fp8_f32 v156, v58, v59 op_sel:[0,0,1]
	v_cvt_pk_fp8_f32 v157, v62, v63 op_sel:[0,0,1]
	s_nop 0
	v_permlane16_swap_b32_e32 v154, v156
	v_permlane16_swap_b32_e32 v155, v157
	global_store_dwordx4 v153, v[154:157], s[8:9] offset:128
	v_pk_fma_f32 v[8:9], v[8:9], v[140:141], v[132:133]
	v_pk_fma_f32 v[10:11], v[10:11], v[142:143], v[134:135]
	v_pk_fma_f32 v[16:17], v[16:17], v[128:129], v[136:137]
	v_pk_fma_f32 v[18:19], v[18:19], v[130:131], v[138:139]
	v_pk_fma_f32 v[24:25], v[24:25], v[140:141], v[132:133]
	v_pk_fma_f32 v[26:27], v[26:27], v[142:143], v[134:135]
	v_pk_fma_f32 v[28:29], v[28:29], v[128:129], v[136:137]
	v_pk_fma_f32 v[30:31], v[30:31], v[130:131], v[138:139]
	v_cvt_pk_fp8_f32 v68, v8, v9
	v_cvt_pk_fp8_f32 v69, v16, v17
	v_cvt_pk_fp8_f32 v70, v24, v25
	v_cvt_pk_fp8_f32 v71, v28, v29
	v_cvt_pk_fp8_f32 v68, v10, v11 op_sel:[0,0,1]
	v_cvt_pk_fp8_f32 v69, v18, v19 op_sel:[0,0,1]
	v_cvt_pk_fp8_f32 v70, v26, v27 op_sel:[0,0,1]
	v_cvt_pk_fp8_f32 v71, v30, v31 op_sel:[0,0,1]
	v_add_u32_e32 v158, 0x8000, v153
	s_nop 0
	v_permlane16_swap_b32_e32 v68, v70
	v_permlane16_swap_b32_e32 v69, v71
	global_store_dwordx4 v158, v[68:71], s[8:9] offset:128
	v_pk_fma_f32 v[32:33], v[32:33], v[140:141], v[132:133]
	v_pk_fma_f32 v[34:35], v[34:35], v[142:143], v[134:135]
	v_pk_fma_f32 v[36:37], v[36:37], v[128:129], v[136:137]
	v_pk_fma_f32 v[38:39], v[38:39], v[130:131], v[138:139]
	v_pk_fma_f32 v[44:45], v[44:45], v[140:141], v[132:133]
	v_pk_fma_f32 v[46:47], v[46:47], v[142:143], v[134:135]
	v_pk_fma_f32 v[52:53], v[52:53], v[128:129], v[136:137]
	v_pk_fma_f32 v[54:55], v[54:55], v[130:131], v[138:139]
	v_cvt_pk_fp8_f32 v154, v32, v33
	v_cvt_pk_fp8_f32 v155, v36, v37
	v_cvt_pk_fp8_f32 v156, v44, v45
	v_cvt_pk_fp8_f32 v157, v52, v53
	v_cvt_pk_fp8_f32 v154, v34, v35 op_sel:[0,0,1]
	v_cvt_pk_fp8_f32 v155, v38, v39 op_sel:[0,0,1]
	v_cvt_pk_fp8_f32 v156, v46, v47 op_sel:[0,0,1]
	v_cvt_pk_fp8_f32 v157, v54, v55 op_sel:[0,0,1]
	v_add_u32_e32 v158, 0x20000, v153
	s_nop 0
	v_permlane16_swap_b32_e32 v154, v156
	v_permlane16_swap_b32_e32 v155, v157
	global_store_dwordx4 v158, v[154:157], s[8:9] offset:128
	v_pk_fma_f32 v[0:1], v[0:1], v[140:141], v[132:133]
	v_pk_fma_f32 v[2:3], v[2:3], v[142:143], v[134:135]
	v_pk_fma_f32 v[4:5], v[4:5], v[128:129], v[136:137]
	v_pk_fma_f32 v[6:7], v[6:7], v[130:131], v[138:139]
	v_pk_fma_f32 v[12:13], v[12:13], v[140:141], v[132:133]
	v_pk_fma_f32 v[14:15], v[14:15], v[142:143], v[134:135]
	v_pk_fma_f32 v[20:21], v[20:21], v[128:129], v[136:137]
	v_pk_fma_f32 v[22:23], v[22:23], v[130:131], v[138:139]
	v_cvt_pk_fp8_f32 v68, v0, v1
	v_cvt_pk_fp8_f32 v69, v4, v5
	v_cvt_pk_fp8_f32 v70, v12, v13
	v_cvt_pk_fp8_f32 v71, v20, v21
	v_cvt_pk_fp8_f32 v68, v2, v3 op_sel:[0,0,1]
	v_cvt_pk_fp8_f32 v69, v6, v7 op_sel:[0,0,1]
	v_cvt_pk_fp8_f32 v70, v14, v15 op_sel:[0,0,1]
	v_cvt_pk_fp8_f32 v71, v22, v23 op_sel:[0,0,1]
	v_add_u32_e32 v158, 0x28000, v153
	s_nop 0
	v_permlane16_swap_b32_e32 v68, v70
	v_permlane16_swap_b32_e32 v69, v71
	global_store_dwordx4 v158, v[68:71], s[8:9] offset:128
	s_mov_b64 s[8:9], -1
	s_andn2_b64 vcc, exec, s[4:5]
	s_cbranch_vccnz .LBB0_1011
	s_andn2_b64 vcc, exec, s[2:3]
	v_mov_b64 v[104:105], 0
	v_mov_b64 v[106:107], 0
	v_mov_b64 v[112:113], 0
	v_mov_b64 v[114:115], 0
	v_mov_b64 v[120:121], 0
	v_mov_b64 v[122:123], 0
	v_mov_b64 v[124:125], 0
	v_mov_b64 v[126:127], 0
	v_mov_b64 v[68:69], 0
	v_mov_b64 v[70:71], 0
	v_mov_b64 v[76:77], 0
	v_mov_b64 v[78:79], 0
	v_mov_b64 v[84:85], 0
	v_mov_b64 v[86:87], 0
	v_mov_b64 v[92:93], 0
	v_mov_b64 v[94:95], 0
	v_mov_b64 v[40:41], 0
	v_mov_b64 v[42:43], 0
	v_mov_b64 v[48:49], 0
	v_mov_b64 v[50:51], 0
	v_mov_b64 v[56:57], 0
	v_mov_b64 v[58:59], 0
	v_mov_b64 v[60:61], 0
	v_mov_b64 v[62:63], 0
	v_mov_b64 v[8:9], 0
	v_mov_b64 v[10:11], 0
	v_mov_b64 v[16:17], 0
	v_mov_b64 v[18:19], 0
	v_mov_b64 v[24:25], 0
	v_mov_b64 v[26:27], 0
	v_mov_b64 v[28:29], 0
	v_mov_b64 v[30:31], 0
	v_mov_b64 v[96:97], 0
	v_mov_b64 v[98:99], 0
	v_mov_b64 v[100:101], 0
	v_mov_b64 v[102:103], 0
	v_mov_b64 v[108:109], 0
	v_mov_b64 v[110:111], 0
	v_mov_b64 v[116:117], 0
	v_mov_b64 v[118:119], 0
	v_mov_b64 v[64:65], 0
	v_mov_b64 v[66:67], 0
	v_mov_b64 v[72:73], 0
	v_mov_b64 v[74:75], 0
	v_mov_b64 v[80:81], 0
	v_mov_b64 v[82:83], 0
	v_mov_b64 v[88:89], 0
	v_mov_b64 v[90:91], 0
	v_mov_b64 v[32:33], 0
	v_mov_b64 v[34:35], 0
	v_mov_b64 v[36:37], 0
	v_mov_b64 v[38:39], 0
	v_mov_b64 v[44:45], 0
	v_mov_b64 v[46:47], 0
	v_mov_b64 v[52:53], 0
	v_mov_b64 v[54:55], 0
	v_mov_b64 v[0:1], 0
	v_mov_b64 v[2:3], 0
	v_mov_b64 v[4:5], 0
	v_mov_b64 v[6:7], 0
	v_mov_b64 v[12:13], 0
	v_mov_b64 v[14:15], 0
	v_mov_b64 v[20:21], 0
	v_mov_b64 v[22:23], 0
	s_cbranch_vccnz .LBB0_1010
	s_barrier
	s_branch .LBB0_1010
